# phase-5 expert-weight conversion bodies rewritten LDS-free (register transpose, dwordx4 loads/stores, two sets, counted vmcnt)
# speedup vs baseline: 1.0084x; 1.0084x over previous
; __device__ __forceinline__ unsigned xb_add(unsigned* p, unsigned v) { return __hip_atomic_fetch_add(p, v, __ATOMIC_RELAXED, __HIP_MEMORY_SCOPE_AGENT); }
;     __device__ __forceinline__ const float* in(int i) const { return *(const float* const __attribute__((address_space(4)))*)(p + 8 * i); }
; __device__ __forceinline__ CvtDesc conv_expert_desc(const KA& a, unsigned char* ws, int q) {
;     const int l = q / Q_PER_L; int r = q - l * Q_PER_L;
;     unsigned char* wl = ws + WS_W + (size_t)l * W_LSTRIDE;
;     CvtDesc d; d.f8 = (MOE_FP8_LAST && (MOE_FP8_GU_ALL || l == NLAYER - 1)) ? 1 : 0;
;     if (MOE_FP8_LAST && MOE_FP8_DOWN_ALL && r >= 2 * Q_IG) d.f8 = 1;
;     const int eb = d.f8 ? 1 : 2;
;     if (r < 2 * Q_IG) { const int up = r >= Q_IG; if (up) r -= Q_IG; const int e = r >> 8, rr = r & 255, kb = rr >> 3, nb = rr & 7, n0 = nb * 64;
;         const float* src = e < 64 ? a.in(up ? 21 : 20) + ((size_t)l * 64 + e) * DM * FFE : a.in(up ? 24 : 23) + (size_t)l * DM * FFE;
;         d.src = src + (size_t)(kb * 64) * FFE + n0; d.N = FFE; d.dKB = DM * eb;
;         d.dst = wl + W_GU + ((size_t)e * 1024 * DM + (size_t)((n0 >> 7) * 256 + up * 128 + (n0 & 127)) * DM + kb * 64) * eb;
;     } else { r -= 2 * Q_IG; const int e = r >> 8, rr = r & 255, kb = rr >> 5, nb = rr & 31;
;         const float* src = e < 64 ? a.in(22) + ((size_t)l * 64 + e) * FFE * DM : a.in(25) + (size_t)l * FFE * DM;
;         d.src = src + (size_t)(kb * 64) * DM + nb * 64; d.N = DM; d.dKB = FFE * eb;
;         d.dst = wl + W_D + ((size_t)e * DM * FFE + (size_t)(nb * 64) * FFE + kb * 64) * eb; }
;     ...
;     for (int nc = 0; nc < max_claims; ++nc) {
;         if (tl == 0) { st[6] = ahead; if (ahead < (unsigned)target && nc + 1 < max_claims) ahead = (ahead + 32u < (unsigned)target) ? xb_add(qw, 32u) : 0xFFFFFFFFu; }
;         __syncthreads();
;         const unsigned base = st[6];
;         if (base < (unsigned)Q_TOTAL) {
;             const int q0 = (int)base + wave; const bool v0 = q0 < Q_TOTAL, v1 = q0 + 8 < Q_TOTAL, v2 = q0 + 16 < Q_TOTAL, v3 = q0 + 24 < Q_TOTAL;
;             float ta[64], tb[64]; CvtDesc da, db;
;             if (v0) { da = conv_expert_desc(a, ws, q0); cvt_load(da, ta, lane); }
;             if (v1) { db = conv_expert_desc(a, ws, q0 + 8); cvt_load(db, tb, lane); }
;             if (v0) cvt_finish(da, ta, scr, lane);
.LBB0_706:
	s_or_b64 exec, exec, s[0:1]
	v_readlane_b32 s0, v254, 27
	s_waitcnt lgkmcnt(0)
	s_barrier
	v_mov_b32_e32 v139, s0
	ds_read_b32 v139, v139
	s_mov_b32 s0, 0x185ff
	s_waitcnt lgkmcnt(0)
	v_cmp_lt_u32_e32 vcc, s0, v139
	v_readfirstlane_b32 s35, v139
	s_cbranch_vccnz .LBB0_779
	s_load_dwordx8 s[12:19], s[6:7], 0xa0
	s_load_dwordx4 s[20:23], s[6:7], 0xc0
	v_mbcnt_lo_u32_b32 v165, -1, 0
	v_mbcnt_hi_u32_b32 v165, -1, v165
	v_lshrrev_b32_e32 v164, 4, v165
	v_and_b32_e32 v165, 15, v165
	s_waitcnt lgkmcnt(0)
	v_writelane_b32 v147, s12, 0
	v_writelane_b32 v147, s13, 1
	v_writelane_b32 v147, s14, 2
	v_writelane_b32 v147, s15, 3
	v_writelane_b32 v147, s16, 4
	v_writelane_b32 v147, s17, 5
	v_writelane_b32 v147, s18, 6
	v_writelane_b32 v147, s19, 7
	v_writelane_b32 v147, s20, 8
	v_writelane_b32 v147, s21, 9
	v_writelane_b32 v147, s22, 10
	v_writelane_b32 v147, s23, 11
	s_add_u32 s38, s35, s26
	s_add_u32 s0, s38, 24
	s_cmp_lt_u32 s0, 0x18600
	s_cbranch_scc0 .Lcv_slow_cv1
	s_mov_b32 s20, s38
	s_cmp_ge_u32 s20, 0xc300
	s_cselect_b32 s21, 1, 0
	s_cselect_b32 s0, 0xc300, 0
	s_sub_u32 s20, s20, s0
	s_cmp_ge_u32 s20, 0x8200
	s_cbranch_scc1 .Lcv_dn0
	s_cmp_ge_u32 s20, 0x4100
	s_cselect_b32 s22, 1, 0
	s_cselect_b32 s0, 0x4100, 0
	s_sub_u32 s20, s20, s0
	s_lshr_b32 s23, s20, 8
	s_lshl_b32 s31, s21, 6
	s_add_u32 s31, s31, s23
	s_cmp_eq_u32 s23, 64
	s_cselect_b32 s0, 3, 0
	s_cselect_b32 s31, s21, s31
	s_add_u32 s0, s0, s22
	s_lshl_b32 s0, s0, 1
	s_nop 0
	v_readlane_b32 s10, v147, s0
	s_or_b32 s0, s0, 1
	s_nop 0
	v_readlane_b32 s11, v147, s0
	s_lshr_b32 s33, s20, 3
	s_and_b32 s33, s33, 31
	s_and_b32 s34, s20, 7
	s_lshl_b32 s0, s33, 17
	s_lshl_b32 s1, s34, 8
	s_or_b32 s0, s0, s1
	s_lshl_b32 s1, s31, 22
	s_or_b32 s0, s0, s1
	s_lshr_b32 s1, s31, 10
	s_add_u32 s10, s10, s0
	s_addc_u32 s11, s11, s1
	s_lshr_b32 s0, s34, 1
	s_lshl_b32 s0, s0, 8
	s_lshl_b32 s1, s22, 7
	s_add_u32 s0, s0, s1
	s_and_b32 s1, s34, 1
	s_lshl_b32 s1, s1, 6
	s_add_u32 s0, s0, s1
	s_lshl_b32 s0, s0, 11
	s_lshl_b32 s1, s33, 6
	s_add_u32 s0, s0, s1
	s_lshl_b32 s1, s23, 21
	s_add_u32 s0, s0, s1
	s_add_u32 s0, s0, 0x2000000
	s_mul_i32 s1, s21, 0x1a800000
	s_add_u32 s0, s0, s1
	s_add_u32 s12, s28, s0
	s_addc_u32 s13, s29, 0
	s_mov_b32 s14, 0
	s_movk_i32 s15, 0x800
	s_mov_b32 s19, 15
	s_branch .Lcv_dd0
.Lcv_dn0:
	s_sub_u32 s20, s20, 0x8200
	s_lshr_b32 s23, s20, 8
	s_lshl_b32 s31, s21, 6
	s_add_u32 s31, s31, s23
	s_cmp_eq_u32 s23, 64
	s_cselect_b32 s0, 5, 2
	s_cselect_b32 s31, s21, s31
	s_lshl_b32 s0, s0, 1
	s_nop 0
	v_readlane_b32 s10, v147, s0
	s_or_b32 s0, s0, 1
	s_nop 0
	v_readlane_b32 s11, v147, s0
	s_lshr_b32 s33, s20, 5
	s_and_b32 s33, s33, 7
	s_and_b32 s34, s20, 31
	s_lshl_b32 s0, s33, 19
	s_lshl_b32 s1, s34, 8
	s_or_b32 s0, s0, s1
	s_lshl_b32 s1, s31, 22
	s_or_b32 s0, s0, s1
	s_lshr_b32 s1, s31, 10
	s_add_u32 s10, s10, s0
	s_addc_u32 s11, s11, s1
	s_lshl_b32 s0, s34, 15
	s_lshl_b32 s1, s33, 6
	s_add_u32 s0, s0, s1
	s_lshl_b32 s1, s23, 20
	s_add_u32 s0, s0, s1
	s_add_u32 s0, s0, 0x12400000
	s_mul_i32 s1, s21, 0x1a800000
	s_add_u32 s0, s0, s1
	s_add_u32 s12, s28, s0
	s_addc_u32 s13, s29, 0
	s_mov_b32 s14, 1
	s_movk_i32 s15, 0x2000
	s_mov_b32 s19, 17
.Lcv_dd0:
	v_lshlrev_b32_e32 v166, 4, v165
	v_lshl_add_u32 v166, v164, s19, v166
	global_load_dwordx4 v[0:3], v166, s[10:11] nt
	v_add_u32_e32 v166, s15, v166
	global_load_dwordx4 v[4:7], v166, s[10:11] nt
	v_add_u32_e32 v166, s15, v166
	global_load_dwordx4 v[8:11], v166, s[10:11] nt
	v_add_u32_e32 v166, s15, v166
	global_load_dwordx4 v[12:15], v166, s[10:11] nt
	v_add_u32_e32 v166, s15, v166
	global_load_dwordx4 v[16:19], v166, s[10:11] nt
	v_add_u32_e32 v166, s15, v166
	global_load_dwordx4 v[20:23], v166, s[10:11] nt
	v_add_u32_e32 v166, s15, v166
	global_load_dwordx4 v[24:27], v166, s[10:11] nt
	v_add_u32_e32 v166, s15, v166
	global_load_dwordx4 v[28:31], v166, s[10:11] nt
	v_add_u32_e32 v166, s15, v166
	global_load_dwordx4 v[32:35], v166, s[10:11] nt
	v_add_u32_e32 v166, s15, v166
	global_load_dwordx4 v[36:39], v166, s[10:11] nt
	v_add_u32_e32 v166, s15, v166
	global_load_dwordx4 v[40:43], v166, s[10:11] nt
	v_add_u32_e32 v166, s15, v166
	global_load_dwordx4 v[44:47], v166, s[10:11] nt
	v_add_u32_e32 v166, s15, v166
	global_load_dwordx4 v[48:51], v166, s[10:11] nt
	v_add_u32_e32 v166, s15, v166
	global_load_dwordx4 v[52:55], v166, s[10:11] nt
	v_add_u32_e32 v166, s15, v166
	global_load_dwordx4 v[56:59], v166, s[10:11] nt
	v_add_u32_e32 v166, s15, v166
	global_load_dwordx4 v[60:63], v166, s[10:11] nt
	s_add_u32 s20, s38, 8
	s_cmp_ge_u32 s20, 0xc300
	s_cselect_b32 s21, 1, 0
	s_cselect_b32 s0, 0xc300, 0
	s_sub_u32 s20, s20, s0
	s_cmp_ge_u32 s20, 0x8200
	s_cbranch_scc1 .Lcv_dn1
	s_cmp_ge_u32 s20, 0x4100
	s_cselect_b32 s22, 1, 0
	s_cselect_b32 s0, 0x4100, 0
	s_sub_u32 s20, s20, s0
	s_lshr_b32 s23, s20, 8
	s_lshl_b32 s31, s21, 6
	s_add_u32 s31, s31, s23
	s_cmp_eq_u32 s23, 64
	s_cselect_b32 s0, 3, 0
	s_cselect_b32 s31, s21, s31
	s_add_u32 s0, s0, s22
	s_lshl_b32 s0, s0, 1
	s_nop 0
	v_readlane_b32 s10, v147, s0
	s_or_b32 s0, s0, 1
	s_nop 0
	v_readlane_b32 s11, v147, s0
	s_lshr_b32 s33, s20, 3
	s_and_b32 s33, s33, 31
	s_and_b32 s34, s20, 7
	s_lshl_b32 s0, s33, 17
	s_lshl_b32 s1, s34, 8
	s_or_b32 s0, s0, s1
	s_lshl_b32 s1, s31, 22
	s_or_b32 s0, s0, s1
	s_lshr_b32 s1, s31, 10
	s_add_u32 s10, s10, s0
	s_addc_u32 s11, s11, s1
	s_lshr_b32 s0, s34, 1
	s_lshl_b32 s0, s0, 8
	s_lshl_b32 s1, s22, 7
	s_add_u32 s0, s0, s1
	s_and_b32 s1, s34, 1
	s_lshl_b32 s1, s1, 6
	s_add_u32 s0, s0, s1
	s_lshl_b32 s0, s0, 11
	s_lshl_b32 s1, s33, 6
	s_add_u32 s0, s0, s1
	s_lshl_b32 s1, s23, 21
	s_add_u32 s0, s0, s1
	s_add_u32 s0, s0, 0x2000000
	s_mul_i32 s1, s21, 0x1a800000
	s_add_u32 s0, s0, s1
	s_add_u32 s16, s28, s0
	s_addc_u32 s17, s29, 0
	s_mov_b32 s18, 0
	s_movk_i32 s15, 0x800
	s_mov_b32 s19, 15
	s_branch .Lcv_dd1
; __device__ __forceinline__ void cvt_load(const CvtDesc& d, float (&t)[64], int lane) {
;     const float* p = d.src + (size_t)(lane >> 4) * d.N + 4 * (lane & 15);
; #pragma unroll
;     for (int i = 0; i < 16; ++i) { const f32x4 v = __builtin_nontemporal_load((const f32x4*)(p + (size_t)(4 * i) * d.N));
;         t[4 * i] = v.x; t[4 * i + 1] = v.y; t[4 * i + 2] = v.z; t[4 * i + 3] = v.w; }
; }
; __device__ __forceinline__ void cvt_finish(const CvtDesc& d, const float (&t)[64], LAS float* scr, int lane) {
;     LAS float* sw = scr + (lane >> 4) * 65 + 4 * (lane & 15);
; #pragma unroll
;     for (int i = 0; i < 16; ++i) { sw[(4 * i) * 65] = t[4 * i]; sw[(4 * i) * 65 + 1] = t[4 * i + 1]; sw[(4 * i) * 65 + 2] = t[4 * i + 2]; sw[(4 * i) * 65 + 3] = t[4 * i + 3]; }
;     LDS_WAIT();
;     const int c = lane & 7;
;     if (d.f8) {
; #pragma unroll
;         for (int j = 0; j < 8; ++j) { const int n = (lane >> 3) + 8 * j; const LAS float* s = scr + (8 * c) * 65 + n;
;             int a = __builtin_amdgcn_cvt_pk_fp8_f32(clamp8(s[0 * 65] * W8_SCALE), clamp8(s[1 * 65] * W8_SCALE), 0, false); a = __builtin_amdgcn_cvt_pk_fp8_f32(clamp8(s[2 * 65] * W8_SCALE), clamp8(s[3 * 65] * W8_SCALE), a, true);
;             int b = __builtin_amdgcn_cvt_pk_fp8_f32(clamp8(s[4 * 65] * W8_SCALE), clamp8(s[5 * 65] * W8_SCALE), 0, false); b = __builtin_amdgcn_cvt_pk_fp8_f32(clamp8(s[6 * 65] * W8_SCALE), clamp8(s[7 * 65] * W8_SCALE), b, true);
;             __builtin_nontemporal_store((u32x2){(unsigned)a, (unsigned)b}, (u32x2*)(d.dst + (size_t)n * d.dKB + 8 * c)); }
; __device__ __forceinline__ CvtDesc conv_expert_desc(const KA& a, unsigned char* ws, int q) {
;     ...
;     if (r < 2 * Q_IG) { const int up = r >= Q_IG; if (up) r -= Q_IG; const int e = r >> 8, rr = r & 255, kb = rr >> 3, nb = rr & 7, n0 = nb * 64;
;         const float* src = e < 64 ? a.in(up ? 21 : 20) + ((size_t)l * 64 + e) * DM * FFE : a.in(up ? 24 : 23) + (size_t)l * DM * FFE;
;         d.src = src + (size_t)(kb * 64) * FFE + n0; d.N = FFE; d.dKB = DM * eb;
;         d.dst = wl + W_GU + ((size_t)e * 1024 * DM + (size_t)((n0 >> 7) * 256 + up * 128 + (n0 & 127)) * DM + kb * 64) * eb;
;     } else { r -= 2 * Q_IG; const int e = r >> 8, rr = r & 255, kb = rr >> 5, nb = rr & 31;
;         const float* src = e < 64 ? a.in(22) + ((size_t)l * 64 + e) * FFE * DM : a.in(25) + (size_t)l * FFE * DM;
.Lcv_dn1:
	s_sub_u32 s20, s20, 0x8200
	s_lshr_b32 s23, s20, 8
	s_lshl_b32 s31, s21, 6
	s_add_u32 s31, s31, s23
	s_cmp_eq_u32 s23, 64
	s_cselect_b32 s0, 5, 2
	s_cselect_b32 s31, s21, s31
	s_lshl_b32 s0, s0, 1
	s_nop 0
	v_readlane_b32 s10, v147, s0
	s_or_b32 s0, s0, 1
	s_nop 0
	v_readlane_b32 s11, v147, s0
	s_lshr_b32 s33, s20, 5
	s_and_b32 s33, s33, 7
	s_and_b32 s34, s20, 31
	s_lshl_b32 s0, s33, 19
	s_lshl_b32 s1, s34, 8
	s_or_b32 s0, s0, s1
	s_lshl_b32 s1, s31, 22
	s_or_b32 s0, s0, s1
	s_lshr_b32 s1, s31, 10
	s_add_u32 s10, s10, s0
	s_addc_u32 s11, s11, s1
	s_lshl_b32 s0, s34, 15
	s_lshl_b32 s1, s33, 6
	s_add_u32 s0, s0, s1
	s_lshl_b32 s1, s23, 20
	s_add_u32 s0, s0, s1
	s_add_u32 s0, s0, 0x12400000
	s_mul_i32 s1, s21, 0x1a800000
	s_add_u32 s0, s0, s1
	s_add_u32 s16, s28, s0
	s_addc_u32 s17, s29, 0
	s_mov_b32 s18, 1
	s_movk_i32 s15, 0x2000
	s_mov_b32 s19, 17
.Lcv_dd1:
	v_lshlrev_b32_e32 v166, 4, v165
	v_lshl_add_u32 v166, v164, s19, v166
	global_load_dwordx4 v[64:67], v166, s[10:11] nt
	v_add_u32_e32 v166, s15, v166
	global_load_dwordx4 v[68:71], v166, s[10:11] nt
	v_add_u32_e32 v166, s15, v166
	global_load_dwordx4 v[72:75], v166, s[10:11] nt
	v_add_u32_e32 v166, s15, v166
	global_load_dwordx4 v[76:79], v166, s[10:11] nt
	v_add_u32_e32 v166, s15, v166
	global_load_dwordx4 v[80:83], v166, s[10:11] nt
	v_add_u32_e32 v166, s15, v166
	global_load_dwordx4 v[84:87], v166, s[10:11] nt
	v_add_u32_e32 v166, s15, v166
	global_load_dwordx4 v[88:91], v166, s[10:11] nt
	v_add_u32_e32 v166, s15, v166
	global_load_dwordx4 v[92:95], v166, s[10:11] nt
	v_add_u32_e32 v166, s15, v166
	global_load_dwordx4 v[96:99], v166, s[10:11] nt
	v_add_u32_e32 v166, s15, v166
	global_load_dwordx4 v[100:103], v166, s[10:11] nt
	v_add_u32_e32 v166, s15, v166
	global_load_dwordx4 v[104:107], v166, s[10:11] nt
	v_add_u32_e32 v166, s15, v166
	global_load_dwordx4 v[108:111], v166, s[10:11] nt
	v_add_u32_e32 v166, s15, v166
	global_load_dwordx4 v[112:115], v166, s[10:11] nt
	v_add_u32_e32 v166, s15, v166
	global_load_dwordx4 v[116:119], v166, s[10:11] nt
	v_add_u32_e32 v166, s15, v166
	global_load_dwordx4 v[120:123], v166, s[10:11] nt
	v_add_u32_e32 v166, s15, v166
	global_load_dwordx4 v[124:127], v166, s[10:11] nt
	s_waitcnt vmcnt(16)
	v_mul_f32_e32 v0, 0x42800000, v0
	v_mul_f32_e32 v1, 0x42800000, v1
	v_mul_f32_e32 v2, 0x42800000, v2
	v_mul_f32_e32 v3, 0x42800000, v3
	v_mul_f32_e32 v4, 0x42800000, v4
	v_mul_f32_e32 v5, 0x42800000, v5
	v_mul_f32_e32 v6, 0x42800000, v6
	v_mul_f32_e32 v7, 0x42800000, v7
	v_mul_f32_e32 v8, 0x42800000, v8
	v_mul_f32_e32 v9, 0x42800000, v9
	v_mul_f32_e32 v10, 0x42800000, v10
	v_mul_f32_e32 v11, 0x42800000, v11
	v_mul_f32_e32 v12, 0x42800000, v12
	v_mul_f32_e32 v13, 0x42800000, v13
	v_mul_f32_e32 v14, 0x42800000, v14
	v_mul_f32_e32 v15, 0x42800000, v15
	v_mul_f32_e32 v16, 0x42800000, v16
	v_mul_f32_e32 v17, 0x42800000, v17
	v_mul_f32_e32 v18, 0x42800000, v18
	v_mul_f32_e32 v19, 0x42800000, v19
	v_mul_f32_e32 v20, 0x42800000, v20
	v_mul_f32_e32 v21, 0x42800000, v21
	v_mul_f32_e32 v22, 0x42800000, v22
	v_mul_f32_e32 v23, 0x42800000, v23
	v_mul_f32_e32 v24, 0x42800000, v24
	v_mul_f32_e32 v25, 0x42800000, v25
	v_mul_f32_e32 v26, 0x42800000, v26
	v_mul_f32_e32 v27, 0x42800000, v27
	v_mul_f32_e32 v28, 0x42800000, v28
	v_mul_f32_e32 v29, 0x42800000, v29
	v_mul_f32_e32 v30, 0x42800000, v30
	v_mul_f32_e32 v31, 0x42800000, v31
	v_mul_f32_e32 v32, 0x42800000, v32
	v_mul_f32_e32 v33, 0x42800000, v33
	v_mul_f32_e32 v34, 0x42800000, v34
	v_mul_f32_e32 v35, 0x42800000, v35
	v_mul_f32_e32 v36, 0x42800000, v36
	v_mul_f32_e32 v37, 0x42800000, v37
	v_mul_f32_e32 v38, 0x42800000, v38
	v_mul_f32_e32 v39, 0x42800000, v39
	v_mul_f32_e32 v40, 0x42800000, v40
	v_mul_f32_e32 v41, 0x42800000, v41
	v_mul_f32_e32 v42, 0x42800000, v42
	v_mul_f32_e32 v43, 0x42800000, v43
	v_mul_f32_e32 v44, 0x42800000, v44
	v_mul_f32_e32 v45, 0x42800000, v45
	v_mul_f32_e32 v46, 0x42800000, v46
	v_mul_f32_e32 v47, 0x42800000, v47
	v_mul_f32_e32 v48, 0x42800000, v48
	v_mul_f32_e32 v49, 0x42800000, v49
	v_mul_f32_e32 v50, 0x42800000, v50
	v_mul_f32_e32 v51, 0x42800000, v51
	v_mul_f32_e32 v52, 0x42800000, v52
	v_mul_f32_e32 v53, 0x42800000, v53
	v_mul_f32_e32 v54, 0x42800000, v54
	v_mul_f32_e32 v55, 0x42800000, v55
	v_mul_f32_e32 v56, 0x42800000, v56
	v_mul_f32_e32 v57, 0x42800000, v57
	v_mul_f32_e32 v58, 0x42800000, v58
	v_mul_f32_e32 v59, 0x42800000, v59
	v_mul_f32_e32 v60, 0x42800000, v60
	v_mul_f32_e32 v61, 0x42800000, v61
	v_mul_f32_e32 v62, 0x42800000, v62
	v_mul_f32_e32 v63, 0x42800000, v63
	v_med3_f32 v0, v0, s93, v224
	v_med3_f32 v1, v1, s93, v224
	v_med3_f32 v2, v2, s93, v224
	v_med3_f32 v3, v3, s93, v224
	v_med3_f32 v4, v4, s93, v224
	v_med3_f32 v5, v5, s93, v224
	v_med3_f32 v6, v6, s93, v224
	v_med3_f32 v7, v7, s93, v224
	v_med3_f32 v8, v8, s93, v224
	v_med3_f32 v9, v9, s93, v224
; __device__ __forceinline__ void cvt_finish(const CvtDesc& d, const float (&t)[64], LAS float* scr, int lane) {
;     LAS float* sw = scr + (lane >> 4) * 65 + 4 * (lane & 15);
; #pragma unroll
;     for (int i = 0; i < 16; ++i) { sw[(4 * i) * 65] = t[4 * i]; sw[(4 * i) * 65 + 1] = t[4 * i + 1]; sw[(4 * i) * 65 + 2] = t[4 * i + 2]; sw[(4 * i) * 65 + 3] = t[4 * i + 3]; }
;     LDS_WAIT();
;     const int c = lane & 7;
;     if (d.f8) {
; #pragma unroll
;         for (int j = 0; j < 8; ++j) { const int n = (lane >> 3) + 8 * j; const LAS float* s = scr + (8 * c) * 65 + n;
;             int a = __builtin_amdgcn_cvt_pk_fp8_f32(clamp8(s[0 * 65] * W8_SCALE), clamp8(s[1 * 65] * W8_SCALE), 0, false); a = __builtin_amdgcn_cvt_pk_fp8_f32(clamp8(s[2 * 65] * W8_SCALE), clamp8(s[3 * 65] * W8_SCALE), a, true);
;             int b = __builtin_amdgcn_cvt_pk_fp8_f32(clamp8(s[4 * 65] * W8_SCALE), clamp8(s[5 * 65] * W8_SCALE), 0, false); b = __builtin_amdgcn_cvt_pk_fp8_f32(clamp8(s[6 * 65] * W8_SCALE), clamp8(s[7 * 65] * W8_SCALE), b, true);
;             __builtin_nontemporal_store((u32x2){(unsigned)a, (unsigned)b}, (u32x2*)(d.dst + (size_t)n * d.dKB + 8 * c)); }
; __device__ __forceinline__ CvtDesc conv_expert_desc(const KA& a, unsigned char* ws, int q) {
;     const int l = q / Q_PER_L; int r = q - l * Q_PER_L;
;     unsigned char* wl = ws + WS_W + (size_t)l * W_LSTRIDE;
;     CvtDesc d; d.f8 = (MOE_FP8_LAST && (MOE_FP8_GU_ALL || l == NLAYER - 1)) ? 1 : 0;
;     if (MOE_FP8_LAST && MOE_FP8_DOWN_ALL && r >= 2 * Q_IG) d.f8 = 1;
;     const int eb = d.f8 ? 1 : 2;
;     if (r < 2 * Q_IG) { const int up = r >= Q_IG; if (up) r -= Q_IG; const int e = r >> 8, rr = r & 255, kb = rr >> 3, nb = rr & 7, n0 = nb * 64;
;         const float* src = e < 64 ? a.in(up ? 21 : 20) + ((size_t)l * 64 + e) * DM * FFE : a.in(up ? 24 : 23) + (size_t)l * DM * FFE;
;         d.src = src + (size_t)(kb * 64) * FFE + n0; d.N = FFE; d.dKB = DM * eb;
;         d.dst = wl + W_GU + ((size_t)e * 1024 * DM + (size_t)((n0 >> 7) * 256 + up * 128 + (n0 & 127)) * DM + kb * 64) * eb;
;     } else { r -= 2 * Q_IG; const int e = r >> 8, rr = r & 255, kb = rr >> 5, nb = rr & 31;
;         const float* src = e < 64 ? a.in(22) + ((size_t)l * 64 + e) * FFE * DM : a.in(25) + (size_t)l * FFE * DM;
;         d.src = src + (size_t)(kb * 64) * DM + nb * 64; d.N = DM; d.dKB = FFE * eb;
	v_med3_f32 v10, v10, s93, v224
	v_med3_f32 v11, v11, s93, v224
	v_med3_f32 v12, v12, s93, v224
	v_med3_f32 v13, v13, s93, v224
	v_med3_f32 v14, v14, s93, v224
	v_med3_f32 v15, v15, s93, v224
	v_med3_f32 v16, v16, s93, v224
	v_med3_f32 v17, v17, s93, v224
	v_med3_f32 v18, v18, s93, v224
	v_med3_f32 v19, v19, s93, v224
	v_med3_f32 v20, v20, s93, v224
	v_med3_f32 v21, v21, s93, v224
	v_med3_f32 v22, v22, s93, v224
	v_med3_f32 v23, v23, s93, v224
	v_med3_f32 v24, v24, s93, v224
	v_med3_f32 v25, v25, s93, v224
	v_med3_f32 v26, v26, s93, v224
	v_med3_f32 v27, v27, s93, v224
	v_med3_f32 v28, v28, s93, v224
	v_med3_f32 v29, v29, s93, v224
	v_med3_f32 v30, v30, s93, v224
	v_med3_f32 v31, v31, s93, v224
	v_med3_f32 v32, v32, s93, v224
	v_med3_f32 v33, v33, s93, v224
	v_med3_f32 v34, v34, s93, v224
	v_med3_f32 v35, v35, s93, v224
	v_med3_f32 v36, v36, s93, v224
	v_med3_f32 v37, v37, s93, v224
	v_med3_f32 v38, v38, s93, v224
	v_med3_f32 v39, v39, s93, v224
	v_med3_f32 v40, v40, s93, v224
	v_med3_f32 v41, v41, s93, v224
	v_med3_f32 v42, v42, s93, v224
	v_med3_f32 v43, v43, s93, v224
	v_med3_f32 v44, v44, s93, v224
	v_med3_f32 v45, v45, s93, v224
	v_med3_f32 v46, v46, s93, v224
	v_med3_f32 v47, v47, s93, v224
	v_med3_f32 v48, v48, s93, v224
	v_med3_f32 v49, v49, s93, v224
	v_med3_f32 v50, v50, s93, v224
	v_med3_f32 v51, v51, s93, v224
	v_med3_f32 v52, v52, s93, v224
	v_med3_f32 v53, v53, s93, v224
	v_med3_f32 v54, v54, s93, v224
	v_med3_f32 v55, v55, s93, v224
	v_med3_f32 v56, v56, s93, v224
	v_med3_f32 v57, v57, s93, v224
	v_med3_f32 v58, v58, s93, v224
	v_med3_f32 v59, v59, s93, v224
	v_med3_f32 v60, v60, s93, v224
	v_med3_f32 v61, v61, s93, v224
	v_med3_f32 v62, v62, s93, v224
	v_med3_f32 v63, v63, s93, v224
	v_cvt_pk_fp8_f32 v148, v0, v4
	v_cvt_pk_fp8_f32 v149, v16, v20
	v_cvt_pk_fp8_f32 v150, v32, v36
	v_cvt_pk_fp8_f32 v151, v48, v52
	v_cvt_pk_fp8_f32 v152, v1, v5
	v_cvt_pk_fp8_f32 v153, v17, v21
	v_cvt_pk_fp8_f32 v154, v33, v37
	v_cvt_pk_fp8_f32 v155, v49, v53
	v_cvt_pk_fp8_f32 v156, v2, v6
	v_cvt_pk_fp8_f32 v157, v18, v22
	v_cvt_pk_fp8_f32 v158, v34, v38
	v_cvt_pk_fp8_f32 v159, v50, v54
	v_cvt_pk_fp8_f32 v160, v3, v7
	v_cvt_pk_fp8_f32 v161, v19, v23
	v_cvt_pk_fp8_f32 v162, v35, v39
	v_cvt_pk_fp8_f32 v163, v51, v55
	v_cvt_pk_fp8_f32 v148, v8, v12 op_sel:[0,0,1]
	v_cvt_pk_fp8_f32 v149, v24, v28 op_sel:[0,0,1]
	v_cvt_pk_fp8_f32 v150, v40, v44 op_sel:[0,0,1]
	v_cvt_pk_fp8_f32 v151, v56, v60 op_sel:[0,0,1]
	v_cvt_pk_fp8_f32 v152, v9, v13 op_sel:[0,0,1]
	v_cvt_pk_fp8_f32 v153, v25, v29 op_sel:[0,0,1]
	v_cvt_pk_fp8_f32 v154, v41, v45 op_sel:[0,0,1]
	v_cvt_pk_fp8_f32 v155, v57, v61 op_sel:[0,0,1]
	v_cvt_pk_fp8_f32 v156, v10, v14 op_sel:[0,0,1]
	v_cvt_pk_fp8_f32 v157, v26, v30 op_sel:[0,0,1]
	v_cvt_pk_fp8_f32 v158, v42, v46 op_sel:[0,0,1]
	v_cvt_pk_fp8_f32 v159, v58, v62 op_sel:[0,0,1]
	v_cvt_pk_fp8_f32 v160, v11, v15 op_sel:[0,0,1]
	v_cvt_pk_fp8_f32 v161, v27, v31 op_sel:[0,0,1]
	v_cvt_pk_fp8_f32 v162, v43, v47 op_sel:[0,0,1]
	v_cvt_pk_fp8_f32 v163, v59, v63 op_sel:[0,0,1]
	s_movk_i32 s1, 0x200
	s_cmp_eq_u32 s14, 0
	s_cselect_b32 s0, 13, 11
	s_cselect_b32 s1, 0x800, s1
	v_lshlrev_b32_e32 v167, 4, v164
	v_lshl_add_u32 v167, v165, s0, v167
	global_store_dwordx4 v167, v[148:151], s[12:13] nt
	v_add_u32_e32 v167, s1, v167
	global_store_dwordx4 v167, v[152:155], s[12:13] nt
	v_add_u32_e32 v167, s1, v167
	global_store_dwordx4 v167, v[156:159], s[12:13] nt
	v_add_u32_e32 v167, s1, v167
	global_store_dwordx4 v167, v[160:163], s[12:13] nt
	s_nop 1
	s_add_u32 s20, s38, 16
	s_cmp_ge_u32 s20, 0xc300
	s_cselect_b32 s21, 1, 0
	s_cselect_b32 s0, 0xc300, 0
	s_sub_u32 s20, s20, s0
	s_cmp_ge_u32 s20, 0x8200
	s_cbranch_scc1 .Lcv_dn2
	s_cmp_ge_u32 s20, 0x4100
	s_cselect_b32 s22, 1, 0
	s_cselect_b32 s0, 0x4100, 0
	s_sub_u32 s20, s20, s0
	s_lshr_b32 s23, s20, 8
	s_lshl_b32 s31, s21, 6
	s_add_u32 s31, s31, s23
	s_cmp_eq_u32 s23, 64
	s_cselect_b32 s0, 3, 0
	s_cselect_b32 s31, s21, s31
	s_add_u32 s0, s0, s22
	s_lshl_b32 s0, s0, 1
	s_nop 0
	v_readlane_b32 s10, v147, s0
	s_or_b32 s0, s0, 1
	s_nop 0
	v_readlane_b32 s11, v147, s0
	s_lshr_b32 s33, s20, 3
	s_and_b32 s33, s33, 31
	s_and_b32 s34, s20, 7
	s_lshl_b32 s0, s33, 17
	s_lshl_b32 s1, s34, 8
	s_or_b32 s0, s0, s1
	s_lshl_b32 s1, s31, 22
	s_or_b32 s0, s0, s1
	s_lshr_b32 s1, s31, 10
	s_add_u32 s10, s10, s0
	s_addc_u32 s11, s11, s1
	s_lshr_b32 s0, s34, 1
	s_lshl_b32 s0, s0, 8
	s_lshl_b32 s1, s22, 7
	s_add_u32 s0, s0, s1
	s_and_b32 s1, s34, 1
	s_lshl_b32 s1, s1, 6
	s_add_u32 s0, s0, s1
	s_lshl_b32 s0, s0, 11
	s_lshl_b32 s1, s33, 6
	s_add_u32 s0, s0, s1
	s_lshl_b32 s1, s23, 21
	s_add_u32 s0, s0, s1
	s_add_u32 s0, s0, 0x2000000
	s_mul_i32 s1, s21, 0x1a800000
	s_add_u32 s0, s0, s1
	s_add_u32 s12, s28, s0
	s_addc_u32 s13, s29, 0
	s_mov_b32 s14, 0
	s_movk_i32 s15, 0x800
	s_mov_b32 s19, 15
	s_branch .Lcv_dd2

; #define LAS __attribute__((address_space(3)))
; __device__ __forceinline__ float clamp8(float x) { return __builtin_amdgcn_fmed3f(x, -448.f, 448.f); }
; #define LDS_WAIT() asm volatile("s_waitcnt lgkmcnt(0)" ::: "memory")
; __device__ __forceinline__ void cvt_load(const CvtDesc& d, float (&t)[64], int lane) {
;     const float* p = d.src + (size_t)(lane >> 4) * d.N + 4 * (lane & 15);
; #pragma unroll
;     for (int i = 0; i < 16; ++i) { const f32x4 v = __builtin_nontemporal_load((const f32x4*)(p + (size_t)(4 * i) * d.N));
;         t[4 * i] = v.x; t[4 * i + 1] = v.y; t[4 * i + 2] = v.z; t[4 * i + 3] = v.w; }
; }
; __device__ __forceinline__ void cvt_finish(const CvtDesc& d, const float (&t)[64], LAS float* scr, int lane) {
;     LAS float* sw = scr + (lane >> 4) * 65 + 4 * (lane & 15);
; #pragma unroll
;     for (int i = 0; i < 16; ++i) { sw[(4 * i) * 65] = t[4 * i]; sw[(4 * i) * 65 + 1] = t[4 * i + 1]; sw[(4 * i) * 65 + 2] = t[4 * i + 2]; sw[(4 * i) * 65 + 3] = t[4 * i + 3]; }
;     LDS_WAIT();
;     const int c = lane & 7;
;     if (d.f8) {
; #pragma unroll
;         for (int j = 0; j < 8; ++j) { const int n = (lane >> 3) + 8 * j; const LAS float* s = scr + (8 * c) * 65 + n;
;             int a = __builtin_amdgcn_cvt_pk_fp8_f32(clamp8(s[0 * 65] * W8_SCALE), clamp8(s[1 * 65] * W8_SCALE), 0, false); a = __builtin_amdgcn_cvt_pk_fp8_f32(clamp8(s[2 * 65] * W8_SCALE), clamp8(s[3 * 65] * W8_SCALE), a, true);
;             int b = __builtin_amdgcn_cvt_pk_fp8_f32(clamp8(s[4 * 65] * W8_SCALE), clamp8(s[5 * 65] * W8_SCALE), 0, false); b = __builtin_amdgcn_cvt_pk_fp8_f32(clamp8(s[6 * 65] * W8_SCALE), clamp8(s[7 * 65] * W8_SCALE), b, true);
.Lcv_dd2:
	v_lshlrev_b32_e32 v166, 4, v165
	v_lshl_add_u32 v166, v164, s19, v166
	global_load_dwordx4 v[0:3], v166, s[10:11] nt
	v_add_u32_e32 v166, s15, v166
	global_load_dwordx4 v[4:7], v166, s[10:11] nt
	v_add_u32_e32 v166, s15, v166
	global_load_dwordx4 v[8:11], v166, s[10:11] nt
	v_add_u32_e32 v166, s15, v166
	global_load_dwordx4 v[12:15], v166, s[10:11] nt
	v_add_u32_e32 v166, s15, v166
	global_load_dwordx4 v[16:19], v166, s[10:11] nt
	v_add_u32_e32 v166, s15, v166
	global_load_dwordx4 v[20:23], v166, s[10:11] nt
	v_add_u32_e32 v166, s15, v166
	global_load_dwordx4 v[24:27], v166, s[10:11] nt
	v_add_u32_e32 v166, s15, v166
	global_load_dwordx4 v[28:31], v166, s[10:11] nt
	v_add_u32_e32 v166, s15, v166
	global_load_dwordx4 v[32:35], v166, s[10:11] nt
	v_add_u32_e32 v166, s15, v166
	global_load_dwordx4 v[36:39], v166, s[10:11] nt
	v_add_u32_e32 v166, s15, v166
	global_load_dwordx4 v[40:43], v166, s[10:11] nt
	v_add_u32_e32 v166, s15, v166
	global_load_dwordx4 v[44:47], v166, s[10:11] nt
	v_add_u32_e32 v166, s15, v166
	global_load_dwordx4 v[48:51], v166, s[10:11] nt
	v_add_u32_e32 v166, s15, v166
	global_load_dwordx4 v[52:55], v166, s[10:11] nt
	v_add_u32_e32 v166, s15, v166
	global_load_dwordx4 v[56:59], v166, s[10:11] nt
	v_add_u32_e32 v166, s15, v166
	global_load_dwordx4 v[60:63], v166, s[10:11] nt
	s_waitcnt vmcnt(20)
	v_mul_f32_e32 v64, 0x42800000, v64
	v_mul_f32_e32 v65, 0x42800000, v65
	v_mul_f32_e32 v66, 0x42800000, v66
	v_mul_f32_e32 v67, 0x42800000, v67
	v_mul_f32_e32 v68, 0x42800000, v68
	v_mul_f32_e32 v69, 0x42800000, v69
	v_mul_f32_e32 v70, 0x42800000, v70
	v_mul_f32_e32 v71, 0x42800000, v71
	v_mul_f32_e32 v72, 0x42800000, v72
	v_mul_f32_e32 v73, 0x42800000, v73
	v_mul_f32_e32 v74, 0x42800000, v74
	v_mul_f32_e32 v75, 0x42800000, v75
	v_mul_f32_e32 v76, 0x42800000, v76
	v_mul_f32_e32 v77, 0x42800000, v77
	v_mul_f32_e32 v78, 0x42800000, v78
	v_mul_f32_e32 v79, 0x42800000, v79
	v_mul_f32_e32 v80, 0x42800000, v80
	v_mul_f32_e32 v81, 0x42800000, v81
	v_mul_f32_e32 v82, 0x42800000, v82
	v_mul_f32_e32 v83, 0x42800000, v83
	v_mul_f32_e32 v84, 0x42800000, v84
	v_mul_f32_e32 v85, 0x42800000, v85
	v_mul_f32_e32 v86, 0x42800000, v86
	v_mul_f32_e32 v87, 0x42800000, v87
	v_mul_f32_e32 v88, 0x42800000, v88
	v_mul_f32_e32 v89, 0x42800000, v89
	v_mul_f32_e32 v90, 0x42800000, v90
	v_mul_f32_e32 v91, 0x42800000, v91
	v_mul_f32_e32 v92, 0x42800000, v92
	v_mul_f32_e32 v93, 0x42800000, v93
	v_mul_f32_e32 v94, 0x42800000, v94
	v_mul_f32_e32 v95, 0x42800000, v95
	v_mul_f32_e32 v96, 0x42800000, v96
	v_mul_f32_e32 v97, 0x42800000, v97
	v_mul_f32_e32 v98, 0x42800000, v98
	v_mul_f32_e32 v99, 0x42800000, v99
	v_mul_f32_e32 v100, 0x42800000, v100
	v_mul_f32_e32 v101, 0x42800000, v101
	v_mul_f32_e32 v102, 0x42800000, v102
	v_mul_f32_e32 v103, 0x42800000, v103
	v_mul_f32_e32 v104, 0x42800000, v104
	v_mul_f32_e32 v105, 0x42800000, v105
	v_mul_f32_e32 v106, 0x42800000, v106
	v_mul_f32_e32 v107, 0x42800000, v107
	v_mul_f32_e32 v108, 0x42800000, v108
	v_mul_f32_e32 v109, 0x42800000, v109
	v_mul_f32_e32 v110, 0x42800000, v110
	v_mul_f32_e32 v111, 0x42800000, v111
	v_mul_f32_e32 v112, 0x42800000, v112
	v_mul_f32_e32 v113, 0x42800000, v113
	v_mul_f32_e32 v114, 0x42800000, v114
	v_mul_f32_e32 v115, 0x42800000, v115
	v_mul_f32_e32 v116, 0x42800000, v116
	v_mul_f32_e32 v117, 0x42800000, v117
	v_mul_f32_e32 v118, 0x42800000, v118
	v_mul_f32_e32 v119, 0x42800000, v119
	v_mul_f32_e32 v120, 0x42800000, v120
	v_mul_f32_e32 v121, 0x42800000, v121
	v_mul_f32_e32 v122, 0x42800000, v122
	v_mul_f32_e32 v123, 0x42800000, v123
	v_mul_f32_e32 v124, 0x42800000, v124
	v_mul_f32_e32 v125, 0x42800000, v125
	v_mul_f32_e32 v126, 0x42800000, v126
	v_mul_f32_e32 v127, 0x42800000, v127
	v_med3_f32 v64, v64, s93, v224
	v_med3_f32 v65, v65, s93, v224
	v_med3_f32 v66, v66, s93, v224
	v_med3_f32 v67, v67, s93, v224
	v_med3_f32 v68, v68, s93, v224
	v_med3_f32 v69, v69, s93, v224
	v_med3_f32 v70, v70, s93, v224
	v_med3_f32 v71, v71, s93, v224
	v_med3_f32 v72, v72, s93, v224
	v_med3_f32 v73, v73, s93, v224
	v_med3_f32 v74, v74, s93, v224
	v_med3_f32 v75, v75, s93, v224
	v_med3_f32 v76, v76, s93, v224
	v_med3_f32 v77, v77, s93, v224
	v_med3_f32 v78, v78, s93, v224
	v_med3_f32 v79, v79, s93, v224
	v_med3_f32 v80, v80, s93, v224
	v_med3_f32 v81, v81, s93, v224
	v_med3_f32 v82, v82, s93, v224
	v_med3_f32 v83, v83, s93, v224
	v_med3_f32 v84, v84, s93, v224
	v_med3_f32 v85, v85, s93, v224
	v_med3_f32 v86, v86, s93, v224
	v_med3_f32 v87, v87, s93, v224
; __device__ __forceinline__ void cvt_finish(const CvtDesc& d, const float (&t)[64], LAS float* scr, int lane) {
;     LAS float* sw = scr + (lane >> 4) * 65 + 4 * (lane & 15);
; #pragma unroll
;     for (int i = 0; i < 16; ++i) { sw[(4 * i) * 65] = t[4 * i]; sw[(4 * i) * 65 + 1] = t[4 * i + 1]; sw[(4 * i) * 65 + 2] = t[4 * i + 2]; sw[(4 * i) * 65 + 3] = t[4 * i + 3]; }
;     LDS_WAIT();
;     const int c = lane & 7;
;     if (d.f8) {
; #pragma unroll
;         for (int j = 0; j < 8; ++j) { const int n = (lane >> 3) + 8 * j; const LAS float* s = scr + (8 * c) * 65 + n;
;             int a = __builtin_amdgcn_cvt_pk_fp8_f32(clamp8(s[0 * 65] * W8_SCALE), clamp8(s[1 * 65] * W8_SCALE), 0, false); a = __builtin_amdgcn_cvt_pk_fp8_f32(clamp8(s[2 * 65] * W8_SCALE), clamp8(s[3 * 65] * W8_SCALE), a, true);
;             int b = __builtin_amdgcn_cvt_pk_fp8_f32(clamp8(s[4 * 65] * W8_SCALE), clamp8(s[5 * 65] * W8_SCALE), 0, false); b = __builtin_amdgcn_cvt_pk_fp8_f32(clamp8(s[6 * 65] * W8_SCALE), clamp8(s[7 * 65] * W8_SCALE), b, true);
;             __builtin_nontemporal_store((u32x2){(unsigned)a, (unsigned)b}, (u32x2*)(d.dst + (size_t)n * d.dKB + 8 * c)); }
; __device__ __forceinline__ CvtDesc conv_expert_desc(const KA& a, unsigned char* ws, int q) {
;     const int l = q / Q_PER_L; int r = q - l * Q_PER_L;
;     unsigned char* wl = ws + WS_W + (size_t)l * W_LSTRIDE;
;     CvtDesc d; d.f8 = (MOE_FP8_LAST && (MOE_FP8_GU_ALL || l == NLAYER - 1)) ? 1 : 0;
;     if (MOE_FP8_LAST && MOE_FP8_DOWN_ALL && r >= 2 * Q_IG) d.f8 = 1;
;     const int eb = d.f8 ? 1 : 2;
;     if (r < 2 * Q_IG) { const int up = r >= Q_IG; if (up) r -= Q_IG; const int e = r >> 8, rr = r & 255, kb = rr >> 3, nb = rr & 7, n0 = nb * 64;
;         const float* src = e < 64 ? a.in(up ? 21 : 20) + ((size_t)l * 64 + e) * DM * FFE : a.in(up ? 24 : 23) + (size_t)l * DM * FFE;
;         d.src = src + (size_t)(kb * 64) * FFE + n0; d.N = FFE; d.dKB = DM * eb;
;         d.dst = wl + W_GU + ((size_t)e * 1024 * DM + (size_t)((n0 >> 7) * 256 + up * 128 + (n0 & 127)) * DM + kb * 64) * eb;
;     } else { r -= 2 * Q_IG; const int e = r >> 8, rr = r & 255, kb = rr >> 5, nb = rr & 31;
;         const float* src = e < 64 ? a.in(22) + ((size_t)l * 64 + e) * FFE * DM : a.in(25) + (size_t)l * FFE * DM;
;         d.src = src + (size_t)(kb * 64) * DM + nb * 64; d.N = DM; d.dKB = FFE * eb;
	v_med3_f32 v88, v88, s93, v224
	v_med3_f32 v89, v89, s93, v224
	v_med3_f32 v90, v90, s93, v224
	v_med3_f32 v91, v91, s93, v224
	v_med3_f32 v92, v92, s93, v224
	v_med3_f32 v93, v93, s93, v224
	v_med3_f32 v94, v94, s93, v224
	v_med3_f32 v95, v95, s93, v224
	v_med3_f32 v96, v96, s93, v224
	v_med3_f32 v97, v97, s93, v224
	v_med3_f32 v98, v98, s93, v224
	v_med3_f32 v99, v99, s93, v224
	v_med3_f32 v100, v100, s93, v224
	v_med3_f32 v101, v101, s93, v224
	v_med3_f32 v102, v102, s93, v224
	v_med3_f32 v103, v103, s93, v224
	v_med3_f32 v104, v104, s93, v224
	v_med3_f32 v105, v105, s93, v224
	v_med3_f32 v106, v106, s93, v224
	v_med3_f32 v107, v107, s93, v224
	v_med3_f32 v108, v108, s93, v224
	v_med3_f32 v109, v109, s93, v224
	v_med3_f32 v110, v110, s93, v224
	v_med3_f32 v111, v111, s93, v224
	v_med3_f32 v112, v112, s93, v224
	v_med3_f32 v113, v113, s93, v224
	v_med3_f32 v114, v114, s93, v224
	v_med3_f32 v115, v115, s93, v224
	v_med3_f32 v116, v116, s93, v224
	v_med3_f32 v117, v117, s93, v224
	v_med3_f32 v118, v118, s93, v224
	v_med3_f32 v119, v119, s93, v224
	v_med3_f32 v120, v120, s93, v224
	v_med3_f32 v121, v121, s93, v224
	v_med3_f32 v122, v122, s93, v224
	v_med3_f32 v123, v123, s93, v224
	v_med3_f32 v124, v124, s93, v224
	v_med3_f32 v125, v125, s93, v224
	v_med3_f32 v126, v126, s93, v224
	v_med3_f32 v127, v127, s93, v224
	v_cvt_pk_fp8_f32 v148, v64, v68
	v_cvt_pk_fp8_f32 v149, v80, v84
	v_cvt_pk_fp8_f32 v150, v96, v100
	v_cvt_pk_fp8_f32 v151, v112, v116
	v_cvt_pk_fp8_f32 v152, v65, v69
	v_cvt_pk_fp8_f32 v153, v81, v85
	v_cvt_pk_fp8_f32 v154, v97, v101
	v_cvt_pk_fp8_f32 v155, v113, v117
	v_cvt_pk_fp8_f32 v156, v66, v70
	v_cvt_pk_fp8_f32 v157, v82, v86
	v_cvt_pk_fp8_f32 v158, v98, v102
	v_cvt_pk_fp8_f32 v159, v114, v118
	v_cvt_pk_fp8_f32 v160, v67, v71
	v_cvt_pk_fp8_f32 v161, v83, v87
	v_cvt_pk_fp8_f32 v162, v99, v103
	v_cvt_pk_fp8_f32 v163, v115, v119
	v_cvt_pk_fp8_f32 v148, v72, v76 op_sel:[0,0,1]
	v_cvt_pk_fp8_f32 v149, v88, v92 op_sel:[0,0,1]
	v_cvt_pk_fp8_f32 v150, v104, v108 op_sel:[0,0,1]
	v_cvt_pk_fp8_f32 v151, v120, v124 op_sel:[0,0,1]
	v_cvt_pk_fp8_f32 v152, v73, v77 op_sel:[0,0,1]
	v_cvt_pk_fp8_f32 v153, v89, v93 op_sel:[0,0,1]
	v_cvt_pk_fp8_f32 v154, v105, v109 op_sel:[0,0,1]
	v_cvt_pk_fp8_f32 v155, v121, v125 op_sel:[0,0,1]
	v_cvt_pk_fp8_f32 v156, v74, v78 op_sel:[0,0,1]
	v_cvt_pk_fp8_f32 v157, v90, v94 op_sel:[0,0,1]
	v_cvt_pk_fp8_f32 v158, v106, v110 op_sel:[0,0,1]
	v_cvt_pk_fp8_f32 v159, v122, v126 op_sel:[0,0,1]
	v_cvt_pk_fp8_f32 v160, v75, v79 op_sel:[0,0,1]
	v_cvt_pk_fp8_f32 v161, v91, v95 op_sel:[0,0,1]
	v_cvt_pk_fp8_f32 v162, v107, v111 op_sel:[0,0,1]
	v_cvt_pk_fp8_f32 v163, v123, v127 op_sel:[0,0,1]
	s_movk_i32 s1, 0x200
	s_cmp_eq_u32 s18, 0
	s_cselect_b32 s0, 13, 11
	s_cselect_b32 s1, 0x800, s1
	v_lshlrev_b32_e32 v167, 4, v164
	v_lshl_add_u32 v167, v165, s0, v167
	global_store_dwordx4 v167, v[148:151], s[16:17] nt
	v_add_u32_e32 v167, s1, v167
	global_store_dwordx4 v167, v[152:155], s[16:17] nt
	v_add_u32_e32 v167, s1, v167
	global_store_dwordx4 v167, v[156:159], s[16:17] nt
	v_add_u32_e32 v167, s1, v167
	global_store_dwordx4 v167, v[160:163], s[16:17] nt
	s_nop 1
	s_add_u32 s20, s38, 24
	s_cmp_ge_u32 s20, 0xc300
	s_cselect_b32 s21, 1, 0
	s_cselect_b32 s0, 0xc300, 0
	s_sub_u32 s20, s20, s0
	s_cmp_ge_u32 s20, 0x8200
	s_cbranch_scc1 .Lcv_dn3
	s_cmp_ge_u32 s20, 0x4100
	s_cselect_b32 s22, 1, 0
	s_cselect_b32 s0, 0x4100, 0
	s_sub_u32 s20, s20, s0
	s_lshr_b32 s23, s20, 8
	s_lshl_b32 s31, s21, 6
	s_add_u32 s31, s31, s23
	s_cmp_eq_u32 s23, 64
	s_cselect_b32 s0, 3, 0
	s_cselect_b32 s31, s21, s31
	s_add_u32 s0, s0, s22
	s_lshl_b32 s0, s0, 1
	s_nop 0
	v_readlane_b32 s10, v147, s0
	s_or_b32 s0, s0, 1
	s_nop 0
	v_readlane_b32 s11, v147, s0
	s_lshr_b32 s33, s20, 3
	s_and_b32 s33, s33, 31
	s_and_b32 s34, s20, 7
	s_lshl_b32 s0, s33, 17
	s_lshl_b32 s1, s34, 8
	s_or_b32 s0, s0, s1
	s_lshl_b32 s1, s31, 22
	s_or_b32 s0, s0, s1
	s_lshr_b32 s1, s31, 10
	s_add_u32 s10, s10, s0
	s_addc_u32 s11, s11, s1
	s_lshr_b32 s0, s34, 1
	s_lshl_b32 s0, s0, 8
	s_lshl_b32 s1, s22, 7
	s_add_u32 s0, s0, s1
	s_and_b32 s1, s34, 1
	s_lshl_b32 s1, s1, 6
	s_add_u32 s0, s0, s1
	s_lshl_b32 s0, s0, 11
	s_lshl_b32 s1, s33, 6
	s_add_u32 s0, s0, s1
	s_lshl_b32 s1, s23, 21
	s_add_u32 s0, s0, s1
	s_add_u32 s0, s0, 0x2000000
	s_mul_i32 s1, s21, 0x1a800000
	s_add_u32 s0, s0, s1
	s_add_u32 s16, s28, s0
	s_addc_u32 s17, s29, 0
	s_mov_b32 s18, 0
	s_movk_i32 s15, 0x800
	s_mov_b32 s19, 15
	s_branch .Lcv_dd3

; #define LAS __attribute__((address_space(3)))
; __device__ __forceinline__ float clamp8(float x) { return __builtin_amdgcn_fmed3f(x, -448.f, 448.f); }
; #define LDS_WAIT() asm volatile("s_waitcnt lgkmcnt(0)" ::: "memory")
; __device__ __forceinline__ void cvt_load(const CvtDesc& d, float (&t)[64], int lane) {
;     const float* p = d.src + (size_t)(lane >> 4) * d.N + 4 * (lane & 15);
; #pragma unroll
;     for (int i = 0; i < 16; ++i) { const f32x4 v = __builtin_nontemporal_load((const f32x4*)(p + (size_t)(4 * i) * d.N));
;         t[4 * i] = v.x; t[4 * i + 1] = v.y; t[4 * i + 2] = v.z; t[4 * i + 3] = v.w; }
; }
; __device__ __forceinline__ void cvt_finish(const CvtDesc& d, const float (&t)[64], LAS float* scr, int lane) {
;     LAS float* sw = scr + (lane >> 4) * 65 + 4 * (lane & 15);
; #pragma unroll
;     for (int i = 0; i < 16; ++i) { sw[(4 * i) * 65] = t[4 * i]; sw[(4 * i) * 65 + 1] = t[4 * i + 1]; sw[(4 * i) * 65 + 2] = t[4 * i + 2]; sw[(4 * i) * 65 + 3] = t[4 * i + 3]; }
;     LDS_WAIT();
;     const int c = lane & 7;
;     if (d.f8) {
; #pragma unroll
;         for (int j = 0; j < 8; ++j) { const int n = (lane >> 3) + 8 * j; const LAS float* s = scr + (8 * c) * 65 + n;
;             int a = __builtin_amdgcn_cvt_pk_fp8_f32(clamp8(s[0 * 65] * W8_SCALE), clamp8(s[1 * 65] * W8_SCALE), 0, false); a = __builtin_amdgcn_cvt_pk_fp8_f32(clamp8(s[2 * 65] * W8_SCALE), clamp8(s[3 * 65] * W8_SCALE), a, true);
;             int b = __builtin_amdgcn_cvt_pk_fp8_f32(clamp8(s[4 * 65] * W8_SCALE), clamp8(s[5 * 65] * W8_SCALE), 0, false); b = __builtin_amdgcn_cvt_pk_fp8_f32(clamp8(s[6 * 65] * W8_SCALE), clamp8(s[7 * 65] * W8_SCALE), b, true);
.Lcv_dd3:
	v_lshlrev_b32_e32 v166, 4, v165
	v_lshl_add_u32 v166, v164, s19, v166
	global_load_dwordx4 v[64:67], v166, s[10:11] nt
	v_add_u32_e32 v166, s15, v166
	global_load_dwordx4 v[68:71], v166, s[10:11] nt
	v_add_u32_e32 v166, s15, v166
	global_load_dwordx4 v[72:75], v166, s[10:11] nt
	v_add_u32_e32 v166, s15, v166
	global_load_dwordx4 v[76:79], v166, s[10:11] nt
	v_add_u32_e32 v166, s15, v166
	global_load_dwordx4 v[80:83], v166, s[10:11] nt
	v_add_u32_e32 v166, s15, v166
	global_load_dwordx4 v[84:87], v166, s[10:11] nt
	v_add_u32_e32 v166, s15, v166
	global_load_dwordx4 v[88:91], v166, s[10:11] nt
	v_add_u32_e32 v166, s15, v166
	global_load_dwordx4 v[92:95], v166, s[10:11] nt
	v_add_u32_e32 v166, s15, v166
	global_load_dwordx4 v[96:99], v166, s[10:11] nt
	v_add_u32_e32 v166, s15, v166
	global_load_dwordx4 v[100:103], v166, s[10:11] nt
	v_add_u32_e32 v166, s15, v166
	global_load_dwordx4 v[104:107], v166, s[10:11] nt
	v_add_u32_e32 v166, s15, v166
	global_load_dwordx4 v[108:111], v166, s[10:11] nt
	v_add_u32_e32 v166, s15, v166
	global_load_dwordx4 v[112:115], v166, s[10:11] nt
	v_add_u32_e32 v166, s15, v166
	global_load_dwordx4 v[116:119], v166, s[10:11] nt
	v_add_u32_e32 v166, s15, v166
	global_load_dwordx4 v[120:123], v166, s[10:11] nt
	v_add_u32_e32 v166, s15, v166
	global_load_dwordx4 v[124:127], v166, s[10:11] nt
	s_waitcnt vmcnt(20)
	v_mul_f32_e32 v0, 0x42800000, v0
	v_mul_f32_e32 v1, 0x42800000, v1
	v_mul_f32_e32 v2, 0x42800000, v2
	v_mul_f32_e32 v3, 0x42800000, v3
	v_mul_f32_e32 v4, 0x42800000, v4
	v_mul_f32_e32 v5, 0x42800000, v5
	v_mul_f32_e32 v6, 0x42800000, v6
	v_mul_f32_e32 v7, 0x42800000, v7
	v_mul_f32_e32 v8, 0x42800000, v8
	v_mul_f32_e32 v9, 0x42800000, v9
	v_mul_f32_e32 v10, 0x42800000, v10
	v_mul_f32_e32 v11, 0x42800000, v11
	v_mul_f32_e32 v12, 0x42800000, v12
	v_mul_f32_e32 v13, 0x42800000, v13
	v_mul_f32_e32 v14, 0x42800000, v14
	v_mul_f32_e32 v15, 0x42800000, v15
	v_mul_f32_e32 v16, 0x42800000, v16
	v_mul_f32_e32 v17, 0x42800000, v17
	v_mul_f32_e32 v18, 0x42800000, v18
	v_mul_f32_e32 v19, 0x42800000, v19
	v_mul_f32_e32 v20, 0x42800000, v20
	v_mul_f32_e32 v21, 0x42800000, v21
	v_mul_f32_e32 v22, 0x42800000, v22
	v_mul_f32_e32 v23, 0x42800000, v23
	v_mul_f32_e32 v24, 0x42800000, v24
	v_mul_f32_e32 v25, 0x42800000, v25
	v_mul_f32_e32 v26, 0x42800000, v26
	v_mul_f32_e32 v27, 0x42800000, v27
	v_mul_f32_e32 v28, 0x42800000, v28
	v_mul_f32_e32 v29, 0x42800000, v29
	v_mul_f32_e32 v30, 0x42800000, v30
	v_mul_f32_e32 v31, 0x42800000, v31
	v_mul_f32_e32 v32, 0x42800000, v32
	v_mul_f32_e32 v33, 0x42800000, v33
	v_mul_f32_e32 v34, 0x42800000, v34
	v_mul_f32_e32 v35, 0x42800000, v35
	v_mul_f32_e32 v36, 0x42800000, v36
	v_mul_f32_e32 v37, 0x42800000, v37
	v_mul_f32_e32 v38, 0x42800000, v38
	v_mul_f32_e32 v39, 0x42800000, v39
	v_mul_f32_e32 v40, 0x42800000, v40
	v_mul_f32_e32 v41, 0x42800000, v41
	v_mul_f32_e32 v42, 0x42800000, v42
	v_mul_f32_e32 v43, 0x42800000, v43
	v_mul_f32_e32 v44, 0x42800000, v44
	v_mul_f32_e32 v45, 0x42800000, v45
	v_mul_f32_e32 v46, 0x42800000, v46
	v_mul_f32_e32 v47, 0x42800000, v47
	v_mul_f32_e32 v48, 0x42800000, v48
	v_mul_f32_e32 v49, 0x42800000, v49
	v_mul_f32_e32 v50, 0x42800000, v50
	v_mul_f32_e32 v51, 0x42800000, v51
	v_mul_f32_e32 v52, 0x42800000, v52
	v_mul_f32_e32 v53, 0x42800000, v53
	v_mul_f32_e32 v54, 0x42800000, v54
	v_mul_f32_e32 v55, 0x42800000, v55
	v_mul_f32_e32 v56, 0x42800000, v56
	v_mul_f32_e32 v57, 0x42800000, v57
	v_mul_f32_e32 v58, 0x42800000, v58
	v_mul_f32_e32 v59, 0x42800000, v59
	v_mul_f32_e32 v60, 0x42800000, v60
	v_mul_f32_e32 v61, 0x42800000, v61
	v_mul_f32_e32 v62, 0x42800000, v62
	v_mul_f32_e32 v63, 0x42800000, v63
	v_med3_f32 v0, v0, s93, v224
	v_med3_f32 v1, v1, s93, v224
	v_med3_f32 v2, v2, s93, v224
	v_med3_f32 v3, v3, s93, v224
	v_med3_f32 v4, v4, s93, v224
	v_med3_f32 v5, v5, s93, v224
	v_med3_f32 v6, v6, s93, v224
	v_med3_f32 v7, v7, s93, v224
	v_med3_f32 v8, v8, s93, v224
	v_med3_f32 v9, v9, s93, v224
	v_med3_f32 v10, v10, s93, v224
	v_med3_f32 v11, v11, s93, v224
	v_med3_f32 v12, v12, s93, v224
	v_med3_f32 v13, v13, s93, v224
	v_med3_f32 v14, v14, s93, v224
	v_med3_f32 v15, v15, s93, v224
	v_med3_f32 v16, v16, s93, v224
	v_med3_f32 v17, v17, s93, v224
	v_med3_f32 v18, v18, s93, v224
	v_med3_f32 v19, v19, s93, v224
	v_med3_f32 v20, v20, s93, v224
	v_med3_f32 v21, v21, s93, v224
	v_med3_f32 v22, v22, s93, v224
	v_med3_f32 v23, v23, s93, v224
	v_med3_f32 v24, v24, s93, v224
	v_med3_f32 v25, v25, s93, v224
	v_med3_f32 v26, v26, s93, v224
	v_med3_f32 v27, v27, s93, v224
	v_med3_f32 v28, v28, s93, v224
	v_med3_f32 v29, v29, s93, v224
	v_med3_f32 v30, v30, s93, v224
	v_med3_f32 v31, v31, s93, v224
	v_med3_f32 v32, v32, s93, v224
	v_med3_f32 v33, v33, s93, v224
	v_med3_f32 v34, v34, s93, v224
	v_med3_f32 v35, v35, s93, v224
	v_med3_f32 v36, v36, s93, v224
	v_med3_f32 v37, v37, s93, v224
	v_med3_f32 v38, v38, s93, v224
	v_med3_f32 v39, v39, s93, v224
	v_med3_f32 v40, v40, s93, v224
	v_med3_f32 v41, v41, s93, v224
	v_med3_f32 v42, v42, s93, v224
	v_med3_f32 v43, v43, s93, v224
	v_med3_f32 v44, v44, s93, v224
	v_med3_f32 v45, v45, s93, v224
	v_med3_f32 v46, v46, s93, v224
	v_med3_f32 v47, v47, s93, v224
	v_med3_f32 v48, v48, s93, v224
	v_med3_f32 v49, v49, s93, v224
	v_med3_f32 v50, v50, s93, v224
	v_med3_f32 v51, v51, s93, v224
	v_med3_f32 v52, v52, s93, v224
	v_med3_f32 v53, v53, s93, v224
	v_med3_f32 v54, v54, s93, v224
	v_med3_f32 v55, v55, s93, v224
	v_med3_f32 v56, v56, s93, v224
	v_med3_f32 v57, v57, s93, v224
	v_med3_f32 v58, v58, s93, v224
	v_med3_f32 v59, v59, s93, v224
	v_med3_f32 v60, v60, s93, v224
	v_med3_f32 v61, v61, s93, v224
	v_med3_f32 v62, v62, s93, v224
; #define LAS __attribute__((address_space(3)))
; __device__ __forceinline__ float clamp8(float x) { return __builtin_amdgcn_fmed3f(x, -448.f, 448.f); }
; #define LDS_WAIT() asm volatile("s_waitcnt lgkmcnt(0)" ::: "memory")
; __device__ __forceinline__ void cvt_finish(const CvtDesc& d, const float (&t)[64], LAS float* scr, int lane) {
;     LAS float* sw = scr + (lane >> 4) * 65 + 4 * (lane & 15);
; #pragma unroll
;     for (int i = 0; i < 16; ++i) { sw[(4 * i) * 65] = t[4 * i]; sw[(4 * i) * 65 + 1] = t[4 * i + 1]; sw[(4 * i) * 65 + 2] = t[4 * i + 2]; sw[(4 * i) * 65 + 3] = t[4 * i + 3]; }
;     LDS_WAIT();
;     const int c = lane & 7;
;     if (d.f8) {
; #pragma unroll
;         for (int j = 0; j < 8; ++j) { const int n = (lane >> 3) + 8 * j; const LAS float* s = scr + (8 * c) * 65 + n;
;             int a = __builtin_amdgcn_cvt_pk_fp8_f32(clamp8(s[0 * 65] * W8_SCALE), clamp8(s[1 * 65] * W8_SCALE), 0, false); a = __builtin_amdgcn_cvt_pk_fp8_f32(clamp8(s[2 * 65] * W8_SCALE), clamp8(s[3 * 65] * W8_SCALE), a, true);
;             int b = __builtin_amdgcn_cvt_pk_fp8_f32(clamp8(s[4 * 65] * W8_SCALE), clamp8(s[5 * 65] * W8_SCALE), 0, false); b = __builtin_amdgcn_cvt_pk_fp8_f32(clamp8(s[6 * 65] * W8_SCALE), clamp8(s[7 * 65] * W8_SCALE), b, true);
;             __builtin_nontemporal_store((u32x2){(unsigned)a, (unsigned)b}, (u32x2*)(d.dst + (size_t)n * d.dKB + 8 * c)); }
	v_med3_f32 v63, v63, s93, v224
	v_cvt_pk_fp8_f32 v148, v0, v4
	v_cvt_pk_fp8_f32 v149, v16, v20
	v_cvt_pk_fp8_f32 v150, v32, v36
	v_cvt_pk_fp8_f32 v151, v48, v52
	v_cvt_pk_fp8_f32 v152, v1, v5
	v_cvt_pk_fp8_f32 v153, v17, v21
	v_cvt_pk_fp8_f32 v154, v33, v37
	v_cvt_pk_fp8_f32 v155, v49, v53
	v_cvt_pk_fp8_f32 v156, v2, v6
	v_cvt_pk_fp8_f32 v157, v18, v22
	v_cvt_pk_fp8_f32 v158, v34, v38
	v_cvt_pk_fp8_f32 v159, v50, v54
	v_cvt_pk_fp8_f32 v160, v3, v7
	v_cvt_pk_fp8_f32 v161, v19, v23
	v_cvt_pk_fp8_f32 v162, v35, v39
	v_cvt_pk_fp8_f32 v163, v51, v55
	v_cvt_pk_fp8_f32 v148, v8, v12 op_sel:[0,0,1]
	v_cvt_pk_fp8_f32 v149, v24, v28 op_sel:[0,0,1]
	v_cvt_pk_fp8_f32 v150, v40, v44 op_sel:[0,0,1]
	v_cvt_pk_fp8_f32 v151, v56, v60 op_sel:[0,0,1]
	v_cvt_pk_fp8_f32 v152, v9, v13 op_sel:[0,0,1]
	v_cvt_pk_fp8_f32 v153, v25, v29 op_sel:[0,0,1]
	v_cvt_pk_fp8_f32 v154, v41, v45 op_sel:[0,0,1]
	v_cvt_pk_fp8_f32 v155, v57, v61 op_sel:[0,0,1]
	v_cvt_pk_fp8_f32 v156, v10, v14 op_sel:[0,0,1]
	v_cvt_pk_fp8_f32 v157, v26, v30 op_sel:[0,0,1]
	v_cvt_pk_fp8_f32 v158, v42, v46 op_sel:[0,0,1]
	v_cvt_pk_fp8_f32 v159, v58, v62 op_sel:[0,0,1]
	v_cvt_pk_fp8_f32 v160, v11, v15 op_sel:[0,0,1]
	v_cvt_pk_fp8_f32 v161, v27, v31 op_sel:[0,0,1]
	v_cvt_pk_fp8_f32 v162, v43, v47 op_sel:[0,0,1]
	v_cvt_pk_fp8_f32 v163, v59, v63 op_sel:[0,0,1]
	s_movk_i32 s1, 0x200
	s_cmp_eq_u32 s14, 0
	s_cselect_b32 s0, 13, 11
	s_cselect_b32 s1, 0x800, s1
	v_lshlrev_b32_e32 v167, 4, v164
	v_lshl_add_u32 v167, v165, s0, v167
	global_store_dwordx4 v167, v[148:151], s[12:13] nt
	v_add_u32_e32 v167, s1, v167
	global_store_dwordx4 v167, v[152:155], s[12:13] nt
	v_add_u32_e32 v167, s1, v167
	global_store_dwordx4 v167, v[156:159], s[12:13] nt
	v_add_u32_e32 v167, s1, v167
	global_store_dwordx4 v167, v[160:163], s[12:13] nt
	s_nop 1
	s_waitcnt vmcnt(4)
	v_mul_f32_e32 v64, 0x42800000, v64
	v_mul_f32_e32 v65, 0x42800000, v65
	v_mul_f32_e32 v66, 0x42800000, v66
	v_mul_f32_e32 v67, 0x42800000, v67
	v_mul_f32_e32 v68, 0x42800000, v68
	v_mul_f32_e32 v69, 0x42800000, v69
	v_mul_f32_e32 v70, 0x42800000, v70
	v_mul_f32_e32 v71, 0x42800000, v71
	v_mul_f32_e32 v72, 0x42800000, v72
	v_mul_f32_e32 v73, 0x42800000, v73
	v_mul_f32_e32 v74, 0x42800000, v74
	v_mul_f32_e32 v75, 0x42800000, v75
	v_mul_f32_e32 v76, 0x42800000, v76
	v_mul_f32_e32 v77, 0x42800000, v77
	v_mul_f32_e32 v78, 0x42800000, v78
	v_mul_f32_e32 v79, 0x42800000, v79
	v_mul_f32_e32 v80, 0x42800000, v80
	v_mul_f32_e32 v81, 0x42800000, v81
	v_mul_f32_e32 v82, 0x42800000, v82
	v_mul_f32_e32 v83, 0x42800000, v83
	v_mul_f32_e32 v84, 0x42800000, v84
	v_mul_f32_e32 v85, 0x42800000, v85
	v_mul_f32_e32 v86, 0x42800000, v86
	v_mul_f32_e32 v87, 0x42800000, v87
	v_mul_f32_e32 v88, 0x42800000, v88
	v_mul_f32_e32 v89, 0x42800000, v89
	v_mul_f32_e32 v90, 0x42800000, v90
	v_mul_f32_e32 v91, 0x42800000, v91
	v_mul_f32_e32 v92, 0x42800000, v92
	v_mul_f32_e32 v93, 0x42800000, v93
	v_mul_f32_e32 v94, 0x42800000, v94
	v_mul_f32_e32 v95, 0x42800000, v95
	v_mul_f32_e32 v96, 0x42800000, v96
	v_mul_f32_e32 v97, 0x42800000, v97
	v_mul_f32_e32 v98, 0x42800000, v98
	v_mul_f32_e32 v99, 0x42800000, v99
	v_mul_f32_e32 v100, 0x42800000, v100
	v_mul_f32_e32 v101, 0x42800000, v101
	v_mul_f32_e32 v102, 0x42800000, v102
	v_mul_f32_e32 v103, 0x42800000, v103
	v_mul_f32_e32 v104, 0x42800000, v104
	v_mul_f32_e32 v105, 0x42800000, v105
	v_mul_f32_e32 v106, 0x42800000, v106
	v_mul_f32_e32 v107, 0x42800000, v107
	v_mul_f32_e32 v108, 0x42800000, v108
	v_mul_f32_e32 v109, 0x42800000, v109
	v_mul_f32_e32 v110, 0x42800000, v110
	v_mul_f32_e32 v111, 0x42800000, v111
	v_mul_f32_e32 v112, 0x42800000, v112
	v_mul_f32_e32 v113, 0x42800000, v113
	v_mul_f32_e32 v114, 0x42800000, v114
	v_mul_f32_e32 v115, 0x42800000, v115
	v_mul_f32_e32 v116, 0x42800000, v116
	v_mul_f32_e32 v117, 0x42800000, v117
	v_mul_f32_e32 v118, 0x42800000, v118
	v_mul_f32_e32 v119, 0x42800000, v119
	v_mul_f32_e32 v120, 0x42800000, v120
	v_mul_f32_e32 v121, 0x42800000, v121
	v_mul_f32_e32 v122, 0x42800000, v122
	v_mul_f32_e32 v123, 0x42800000, v123
	v_mul_f32_e32 v124, 0x42800000, v124
	v_mul_f32_e32 v125, 0x42800000, v125
	v_mul_f32_e32 v126, 0x42800000, v126
	v_mul_f32_e32 v127, 0x42800000, v127
	v_med3_f32 v64, v64, s93, v224
	v_med3_f32 v65, v65, s93, v224
	v_med3_f32 v66, v66, s93, v224
	v_med3_f32 v67, v67, s93, v224
	v_med3_f32 v68, v68, s93, v224
	v_med3_f32 v69, v69, s93, v224
	v_med3_f32 v70, v70, s93, v224
	v_med3_f32 v71, v71, s93, v224
	v_med3_f32 v72, v72, s93, v224
	v_med3_f32 v73, v73, s93, v224
	v_med3_f32 v74, v74, s93, v224
	v_med3_f32 v75, v75, s93, v224
	v_med3_f32 v76, v76, s93, v224
	v_med3_f32 v77, v77, s93, v224
	v_med3_f32 v78, v78, s93, v224
	v_med3_f32 v79, v79, s93, v224
	v_med3_f32 v80, v80, s93, v224
	v_med3_f32 v81, v81, s93, v224
; #define LAS __attribute__((address_space(3)))
; __device__ __forceinline__ float clamp8(float x) { return __builtin_amdgcn_fmed3f(x, -448.f, 448.f); }
; #define LDS_WAIT() asm volatile("s_waitcnt lgkmcnt(0)" ::: "memory")
;     __device__ __forceinline__ unsigned char* ws() const { return *(unsigned char* const __attribute__((address_space(4)))*)(p + 232); }
; __device__ __forceinline__ void cvt_finish(const CvtDesc& d, const float (&t)[64], LAS float* scr, int lane) {
;     LAS float* sw = scr + (lane >> 4) * 65 + 4 * (lane & 15);
; #pragma unroll
;     for (int i = 0; i < 16; ++i) { sw[(4 * i) * 65] = t[4 * i]; sw[(4 * i) * 65 + 1] = t[4 * i + 1]; sw[(4 * i) * 65 + 2] = t[4 * i + 2]; sw[(4 * i) * 65 + 3] = t[4 * i + 3]; }
;     LDS_WAIT();
;     const int c = lane & 7;
;     if (d.f8) {
; #pragma unroll
;         for (int j = 0; j < 8; ++j) { const int n = (lane >> 3) + 8 * j; const LAS float* s = scr + (8 * c) * 65 + n;
;             int a = __builtin_amdgcn_cvt_pk_fp8_f32(clamp8(s[0 * 65] * W8_SCALE), clamp8(s[1 * 65] * W8_SCALE), 0, false); a = __builtin_amdgcn_cvt_pk_fp8_f32(clamp8(s[2 * 65] * W8_SCALE), clamp8(s[3 * 65] * W8_SCALE), a, true);
;             int b = __builtin_amdgcn_cvt_pk_fp8_f32(clamp8(s[4 * 65] * W8_SCALE), clamp8(s[5 * 65] * W8_SCALE), 0, false); b = __builtin_amdgcn_cvt_pk_fp8_f32(clamp8(s[6 * 65] * W8_SCALE), clamp8(s[7 * 65] * W8_SCALE), b, true);
;             __builtin_nontemporal_store((u32x2){(unsigned)a, (unsigned)b}, (u32x2*)(d.dst + (size_t)n * d.dKB + 8 * c)); }
;     ...
;         if (base < (unsigned)Q_TOTAL) {
;             const int q0 = (int)base + wave; const bool v0 = q0 < Q_TOTAL, v1 = q0 + 8 < Q_TOTAL, v2 = q0 + 16 < Q_TOTAL, v3 = q0 + 24 < Q_TOTAL;
;             float ta[64], tb[64]; CvtDesc da, db;
;             if (v0) { da = conv_expert_desc(a, ws, q0); cvt_load(da, ta, lane); }
;             if (v1) { db = conv_expert_desc(a, ws, q0 + 8); cvt_load(db, tb, lane); }
;             if (v0) cvt_finish(da, ta, scr, lane);
;             if (v2) { da = conv_expert_desc(a, ws, q0 + 16); cvt_load(da, ta, lane); }
;             if (v1) cvt_finish(db, tb, scr, lane);
;             if (v3) { db = conv_expert_desc(a, ws, q0 + 24); cvt_load(db, tb, lane); }
;             if (v2) cvt_finish(da, ta, scr, lane);
;             if (v3) cvt_finish(db, tb, scr, lane);
	v_med3_f32 v82, v82, s93, v224
	v_med3_f32 v83, v83, s93, v224
	v_med3_f32 v84, v84, s93, v224
	v_med3_f32 v85, v85, s93, v224
	v_med3_f32 v86, v86, s93, v224
	v_med3_f32 v87, v87, s93, v224
	v_med3_f32 v88, v88, s93, v224
	v_med3_f32 v89, v89, s93, v224
	v_med3_f32 v90, v90, s93, v224
	v_med3_f32 v91, v91, s93, v224
	v_med3_f32 v92, v92, s93, v224
	v_med3_f32 v93, v93, s93, v224
	v_med3_f32 v94, v94, s93, v224
	v_med3_f32 v95, v95, s93, v224
	v_med3_f32 v96, v96, s93, v224
	v_med3_f32 v97, v97, s93, v224
	v_med3_f32 v98, v98, s93, v224
	v_med3_f32 v99, v99, s93, v224
	v_med3_f32 v100, v100, s93, v224
	v_med3_f32 v101, v101, s93, v224
	v_med3_f32 v102, v102, s93, v224
	v_med3_f32 v103, v103, s93, v224
	v_med3_f32 v104, v104, s93, v224
	v_med3_f32 v105, v105, s93, v224
	v_med3_f32 v106, v106, s93, v224
	v_med3_f32 v107, v107, s93, v224
	v_med3_f32 v108, v108, s93, v224
	v_med3_f32 v109, v109, s93, v224
	v_med3_f32 v110, v110, s93, v224
	v_med3_f32 v111, v111, s93, v224
	v_med3_f32 v112, v112, s93, v224
	v_med3_f32 v113, v113, s93, v224
	v_med3_f32 v114, v114, s93, v224
	v_med3_f32 v115, v115, s93, v224
	v_med3_f32 v116, v116, s93, v224
	v_med3_f32 v117, v117, s93, v224
	v_med3_f32 v118, v118, s93, v224
	v_med3_f32 v119, v119, s93, v224
	v_med3_f32 v120, v120, s93, v224
	v_med3_f32 v121, v121, s93, v224
	v_med3_f32 v122, v122, s93, v224
	v_med3_f32 v123, v123, s93, v224
	v_med3_f32 v124, v124, s93, v224
	v_med3_f32 v125, v125, s93, v224
	v_med3_f32 v126, v126, s93, v224
	v_med3_f32 v127, v127, s93, v224
	v_cvt_pk_fp8_f32 v148, v64, v68
	v_cvt_pk_fp8_f32 v149, v80, v84
	v_cvt_pk_fp8_f32 v150, v96, v100
	v_cvt_pk_fp8_f32 v151, v112, v116
	v_cvt_pk_fp8_f32 v152, v65, v69
	v_cvt_pk_fp8_f32 v153, v81, v85
	v_cvt_pk_fp8_f32 v154, v97, v101
	v_cvt_pk_fp8_f32 v155, v113, v117
	v_cvt_pk_fp8_f32 v156, v66, v70
	v_cvt_pk_fp8_f32 v157, v82, v86
	v_cvt_pk_fp8_f32 v158, v98, v102
	v_cvt_pk_fp8_f32 v159, v114, v118
	v_cvt_pk_fp8_f32 v160, v67, v71
	v_cvt_pk_fp8_f32 v161, v83, v87
	v_cvt_pk_fp8_f32 v162, v99, v103
	v_cvt_pk_fp8_f32 v163, v115, v119
	v_cvt_pk_fp8_f32 v148, v72, v76 op_sel:[0,0,1]
	v_cvt_pk_fp8_f32 v149, v88, v92 op_sel:[0,0,1]
	v_cvt_pk_fp8_f32 v150, v104, v108 op_sel:[0,0,1]
	v_cvt_pk_fp8_f32 v151, v120, v124 op_sel:[0,0,1]
	v_cvt_pk_fp8_f32 v152, v73, v77 op_sel:[0,0,1]
	v_cvt_pk_fp8_f32 v153, v89, v93 op_sel:[0,0,1]
	v_cvt_pk_fp8_f32 v154, v105, v109 op_sel:[0,0,1]
	v_cvt_pk_fp8_f32 v155, v121, v125 op_sel:[0,0,1]
	v_cvt_pk_fp8_f32 v156, v74, v78 op_sel:[0,0,1]
	v_cvt_pk_fp8_f32 v157, v90, v94 op_sel:[0,0,1]
	v_cvt_pk_fp8_f32 v158, v106, v110 op_sel:[0,0,1]
	v_cvt_pk_fp8_f32 v159, v122, v126 op_sel:[0,0,1]
	v_cvt_pk_fp8_f32 v160, v75, v79 op_sel:[0,0,1]
	v_cvt_pk_fp8_f32 v161, v91, v95 op_sel:[0,0,1]
	v_cvt_pk_fp8_f32 v162, v107, v111 op_sel:[0,0,1]
	v_cvt_pk_fp8_f32 v163, v123, v127 op_sel:[0,0,1]
	s_movk_i32 s1, 0x200
	s_cmp_eq_u32 s18, 0
	s_cselect_b32 s0, 13, 11
	s_cselect_b32 s1, 0x800, s1
	v_lshlrev_b32_e32 v167, 4, v164
	v_lshl_add_u32 v167, v165, s0, v167
	global_store_dwordx4 v167, v[148:151], s[16:17] nt
	v_add_u32_e32 v167, s1, v167
	global_store_dwordx4 v167, v[152:155], s[16:17] nt
	v_add_u32_e32 v167, s1, v167
	global_store_dwordx4 v167, v[156:159], s[16:17] nt
	v_add_u32_e32 v167, s1, v167
	global_store_dwordx4 v167, v[160:163], s[16:17] nt
	s_nop 1
	s_branch .LBB0_779
.Lcv_slow_cv1:
	s_mov_b32 s68, 0
.Lcv_sl_cv1:
	s_lshl_b32 s0, s68, 3
	s_add_u32 s20, s38, s0
	s_cmp_lt_u32 s20, 0x18600
	s_cbranch_scc0 .LBB0_779
	s_cmp_ge_u32 s20, 0xc300
	s_cselect_b32 s21, 1, 0
	s_cselect_b32 s0, 0xc300, 0
	s_sub_u32 s20, s20, s0
	s_cmp_ge_u32 s20, 0x8200
	s_cbranch_scc1 .Lcv_dn4
	s_cmp_ge_u32 s20, 0x4100
	s_cselect_b32 s22, 1, 0
	s_cselect_b32 s0, 0x4100, 0
	s_sub_u32 s20, s20, s0
	s_lshr_b32 s23, s20, 8
	s_lshl_b32 s31, s21, 6
	s_add_u32 s31, s31, s23
	s_cmp_eq_u32 s23, 64
	s_cselect_b32 s0, 3, 0
	s_cselect_b32 s31, s21, s31
	s_add_u32 s0, s0, s22
	s_lshl_b32 s0, s0, 1
	s_nop 0
	v_readlane_b32 s10, v147, s0
	s_or_b32 s0, s0, 1
	s_nop 0
	v_readlane_b32 s11, v147, s0
	s_lshr_b32 s33, s20, 3
	s_and_b32 s33, s33, 31
	s_and_b32 s34, s20, 7
	s_lshl_b32 s0, s33, 17
	s_lshl_b32 s1, s34, 8
	s_or_b32 s0, s0, s1
	s_lshl_b32 s1, s31, 22
	s_or_b32 s0, s0, s1
	s_lshr_b32 s1, s31, 10
	s_add_u32 s10, s10, s0
	s_addc_u32 s11, s11, s1
	s_lshr_b32 s0, s34, 1
	s_lshl_b32 s0, s0, 8
	s_lshl_b32 s1, s22, 7
	s_add_u32 s0, s0, s1
	s_and_b32 s1, s34, 1
	s_lshl_b32 s1, s1, 6
	s_add_u32 s0, s0, s1
	s_lshl_b32 s0, s0, 11
	s_lshl_b32 s1, s33, 6
	s_add_u32 s0, s0, s1
	s_lshl_b32 s1, s23, 21
	s_add_u32 s0, s0, s1
	s_add_u32 s0, s0, 0x2000000
	s_mul_i32 s1, s21, 0x1a800000
	s_add_u32 s0, s0, s1
	s_add_u32 s12, s28, s0
	s_addc_u32 s13, s29, 0
	s_mov_b32 s14, 0
	s_movk_i32 s15, 0x800
	s_mov_b32 s19, 15
	s_branch .Lcv_dd4

; __device__ __forceinline__ void cvt_load(const CvtDesc& d, float (&t)[64], int lane) {
;     const float* p = d.src + (size_t)(lane >> 4) * d.N + 4 * (lane & 15);
; #pragma unroll
;     for (int i = 0; i < 16; ++i) { const f32x4 v = __builtin_nontemporal_load((const f32x4*)(p + (size_t)(4 * i) * d.N));
;         t[4 * i] = v.x; t[4 * i + 1] = v.y; t[4 * i + 2] = v.z; t[4 * i + 3] = v.w; }
; }
.Lcv_dd4:
	v_lshlrev_b32_e32 v166, 4, v165
	v_lshl_add_u32 v166, v164, s19, v166
	global_load_dwordx4 v[0:3], v166, s[10:11] nt
	v_add_u32_e32 v166, s15, v166
	global_load_dwordx4 v[4:7], v166, s[10:11] nt
	v_add_u32_e32 v166, s15, v166
	global_load_dwordx4 v[8:11], v166, s[10:11] nt
	v_add_u32_e32 v166, s15, v166
	global_load_dwordx4 v[12:15], v166, s[10:11] nt
	v_add_u32_e32 v166, s15, v166
	global_load_dwordx4 v[16:19], v166, s[10:11] nt
	v_add_u32_e32 v166, s15, v166
	global_load_dwordx4 v[20:23], v166, s[10:11] nt
	v_add_u32_e32 v166, s15, v166
	global_load_dwordx4 v[24:27], v166, s[10:11] nt
	v_add_u32_e32 v166, s15, v166
	global_load_dwordx4 v[28:31], v166, s[10:11] nt
	v_add_u32_e32 v166, s15, v166
	global_load_dwordx4 v[32:35], v166, s[10:11] nt
	v_add_u32_e32 v166, s15, v166
	global_load_dwordx4 v[36:39], v166, s[10:11] nt
	v_add_u32_e32 v166, s15, v166
	global_load_dwordx4 v[40:43], v166, s[10:11] nt
	v_add_u32_e32 v166, s15, v166
	global_load_dwordx4 v[44:47], v166, s[10:11] nt
	v_add_u32_e32 v166, s15, v166
	global_load_dwordx4 v[48:51], v166, s[10:11] nt
	v_add_u32_e32 v166, s15, v166
	global_load_dwordx4 v[52:55], v166, s[10:11] nt
	v_add_u32_e32 v166, s15, v166
	global_load_dwordx4 v[56:59], v166, s[10:11] nt
	v_add_u32_e32 v166, s15, v166
	global_load_dwordx4 v[60:63], v166, s[10:11] nt
	s_waitcnt vmcnt(0)
; #define LAS __attribute__((address_space(3)))
; __device__ __forceinline__ float clamp8(float x) { return __builtin_amdgcn_fmed3f(x, -448.f, 448.f); }
; #define LDS_WAIT() asm volatile("s_waitcnt lgkmcnt(0)" ::: "memory")
; __device__ __forceinline__ void cvt_finish(const CvtDesc& d, const float (&t)[64], LAS float* scr, int lane) {
;     LAS float* sw = scr + (lane >> 4) * 65 + 4 * (lane & 15);
; #pragma unroll
;     for (int i = 0; i < 16; ++i) { sw[(4 * i) * 65] = t[4 * i]; sw[(4 * i) * 65 + 1] = t[4 * i + 1]; sw[(4 * i) * 65 + 2] = t[4 * i + 2]; sw[(4 * i) * 65 + 3] = t[4 * i + 3]; }
;     LDS_WAIT();
;     const int c = lane & 7;
;     if (d.f8) {
; #pragma unroll
;         for (int j = 0; j < 8; ++j) { const int n = (lane >> 3) + 8 * j; const LAS float* s = scr + (8 * c) * 65 + n;
;             int a = __builtin_amdgcn_cvt_pk_fp8_f32(clamp8(s[0 * 65] * W8_SCALE), clamp8(s[1 * 65] * W8_SCALE), 0, false); a = __builtin_amdgcn_cvt_pk_fp8_f32(clamp8(s[2 * 65] * W8_SCALE), clamp8(s[3 * 65] * W8_SCALE), a, true);
;             int b = __builtin_amdgcn_cvt_pk_fp8_f32(clamp8(s[4 * 65] * W8_SCALE), clamp8(s[5 * 65] * W8_SCALE), 0, false); b = __builtin_amdgcn_cvt_pk_fp8_f32(clamp8(s[6 * 65] * W8_SCALE), clamp8(s[7 * 65] * W8_SCALE), b, true);
;             __builtin_nontemporal_store((u32x2){(unsigned)a, (unsigned)b}, (u32x2*)(d.dst + (size_t)n * d.dKB + 8 * c)); }
	v_mul_f32_e32 v0, 0x42800000, v0
	v_mul_f32_e32 v1, 0x42800000, v1
	v_mul_f32_e32 v2, 0x42800000, v2
	v_mul_f32_e32 v3, 0x42800000, v3
	v_mul_f32_e32 v4, 0x42800000, v4
	v_mul_f32_e32 v5, 0x42800000, v5
	v_mul_f32_e32 v6, 0x42800000, v6
	v_mul_f32_e32 v7, 0x42800000, v7
	v_mul_f32_e32 v8, 0x42800000, v8
	v_mul_f32_e32 v9, 0x42800000, v9
	v_mul_f32_e32 v10, 0x42800000, v10
	v_mul_f32_e32 v11, 0x42800000, v11
	v_mul_f32_e32 v12, 0x42800000, v12
	v_mul_f32_e32 v13, 0x42800000, v13
	v_mul_f32_e32 v14, 0x42800000, v14
	v_mul_f32_e32 v15, 0x42800000, v15
	v_mul_f32_e32 v16, 0x42800000, v16
	v_mul_f32_e32 v17, 0x42800000, v17
	v_mul_f32_e32 v18, 0x42800000, v18
	v_mul_f32_e32 v19, 0x42800000, v19
	v_mul_f32_e32 v20, 0x42800000, v20
	v_mul_f32_e32 v21, 0x42800000, v21
	v_mul_f32_e32 v22, 0x42800000, v22
	v_mul_f32_e32 v23, 0x42800000, v23
	v_mul_f32_e32 v24, 0x42800000, v24
	v_mul_f32_e32 v25, 0x42800000, v25
	v_mul_f32_e32 v26, 0x42800000, v26
	v_mul_f32_e32 v27, 0x42800000, v27
	v_mul_f32_e32 v28, 0x42800000, v28
	v_mul_f32_e32 v29, 0x42800000, v29
	v_mul_f32_e32 v30, 0x42800000, v30
	v_mul_f32_e32 v31, 0x42800000, v31
	v_mul_f32_e32 v32, 0x42800000, v32
	v_mul_f32_e32 v33, 0x42800000, v33
	v_mul_f32_e32 v34, 0x42800000, v34
	v_mul_f32_e32 v35, 0x42800000, v35
	v_mul_f32_e32 v36, 0x42800000, v36
	v_mul_f32_e32 v37, 0x42800000, v37
	v_mul_f32_e32 v38, 0x42800000, v38
	v_mul_f32_e32 v39, 0x42800000, v39
	v_mul_f32_e32 v40, 0x42800000, v40
	v_mul_f32_e32 v41, 0x42800000, v41
	v_mul_f32_e32 v42, 0x42800000, v42
	v_mul_f32_e32 v43, 0x42800000, v43
	v_mul_f32_e32 v44, 0x42800000, v44
	v_mul_f32_e32 v45, 0x42800000, v45
	v_mul_f32_e32 v46, 0x42800000, v46
	v_mul_f32_e32 v47, 0x42800000, v47
	v_mul_f32_e32 v48, 0x42800000, v48
	v_mul_f32_e32 v49, 0x42800000, v49
	v_mul_f32_e32 v50, 0x42800000, v50
	v_mul_f32_e32 v51, 0x42800000, v51
	v_mul_f32_e32 v52, 0x42800000, v52
	v_mul_f32_e32 v53, 0x42800000, v53
	v_mul_f32_e32 v54, 0x42800000, v54
	v_mul_f32_e32 v55, 0x42800000, v55
	v_mul_f32_e32 v56, 0x42800000, v56
	v_mul_f32_e32 v57, 0x42800000, v57
	v_mul_f32_e32 v58, 0x42800000, v58
	v_mul_f32_e32 v59, 0x42800000, v59
	v_mul_f32_e32 v60, 0x42800000, v60
	v_mul_f32_e32 v61, 0x42800000, v61
	v_mul_f32_e32 v62, 0x42800000, v62
	v_mul_f32_e32 v63, 0x42800000, v63
	v_med3_f32 v0, v0, s93, v224
	v_med3_f32 v1, v1, s93, v224
	v_med3_f32 v2, v2, s93, v224
	v_med3_f32 v3, v3, s93, v224
	v_med3_f32 v4, v4, s93, v224
	v_med3_f32 v5, v5, s93, v224
	v_med3_f32 v6, v6, s93, v224
	v_med3_f32 v7, v7, s93, v224
	v_med3_f32 v8, v8, s93, v224
	v_med3_f32 v9, v9, s93, v224
	v_med3_f32 v10, v10, s93, v224
	v_med3_f32 v11, v11, s93, v224
	v_med3_f32 v12, v12, s93, v224
	v_med3_f32 v13, v13, s93, v224
	v_med3_f32 v14, v14, s93, v224
	v_med3_f32 v15, v15, s93, v224
	v_med3_f32 v16, v16, s93, v224
	v_med3_f32 v17, v17, s93, v224
	v_med3_f32 v18, v18, s93, v224
	v_med3_f32 v19, v19, s93, v224
	v_med3_f32 v20, v20, s93, v224
	v_med3_f32 v21, v21, s93, v224
	v_med3_f32 v22, v22, s93, v224
	v_med3_f32 v23, v23, s93, v224
	v_med3_f32 v24, v24, s93, v224
	v_med3_f32 v25, v25, s93, v224
	v_med3_f32 v26, v26, s93, v224
	v_med3_f32 v27, v27, s93, v224
	v_med3_f32 v28, v28, s93, v224
	v_med3_f32 v29, v29, s93, v224
	v_med3_f32 v30, v30, s93, v224
	v_med3_f32 v31, v31, s93, v224
	v_med3_f32 v32, v32, s93, v224
	v_med3_f32 v33, v33, s93, v224
	v_med3_f32 v34, v34, s93, v224
	v_med3_f32 v35, v35, s93, v224
	v_med3_f32 v36, v36, s93, v224
	v_med3_f32 v37, v37, s93, v224
	v_med3_f32 v38, v38, s93, v224
	v_med3_f32 v39, v39, s93, v224
	v_med3_f32 v40, v40, s93, v224
	v_med3_f32 v41, v41, s93, v224
	v_med3_f32 v42, v42, s93, v224
	v_med3_f32 v43, v43, s93, v224
	v_med3_f32 v44, v44, s93, v224
	v_med3_f32 v45, v45, s93, v224
	v_med3_f32 v46, v46, s93, v224
	v_med3_f32 v47, v47, s93, v224
	v_med3_f32 v48, v48, s93, v224
	v_med3_f32 v49, v49, s93, v224
	v_med3_f32 v50, v50, s93, v224
	v_med3_f32 v51, v51, s93, v224
	v_med3_f32 v52, v52, s93, v224
	v_med3_f32 v53, v53, s93, v224
	v_med3_f32 v54, v54, s93, v224
	v_med3_f32 v55, v55, s93, v224
	v_med3_f32 v56, v56, s93, v224
	v_med3_f32 v57, v57, s93, v224
	v_med3_f32 v58, v58, s93, v224
	v_med3_f32 v59, v59, s93, v224
	v_med3_f32 v60, v60, s93, v224
	v_med3_f32 v61, v61, s93, v224
	v_med3_f32 v62, v62, s93, v224
	v_med3_f32 v63, v63, s93, v224
	v_cvt_pk_fp8_f32 v148, v0, v4
	v_cvt_pk_fp8_f32 v149, v16, v20
	v_cvt_pk_fp8_f32 v150, v32, v36
	v_cvt_pk_fp8_f32 v151, v48, v52
	v_cvt_pk_fp8_f32 v152, v1, v5
	v_cvt_pk_fp8_f32 v153, v17, v21
	v_cvt_pk_fp8_f32 v154, v33, v37
	v_cvt_pk_fp8_f32 v155, v49, v53
	v_cvt_pk_fp8_f32 v156, v2, v6
	v_cvt_pk_fp8_f32 v157, v18, v22
	v_cvt_pk_fp8_f32 v158, v34, v38
	v_cvt_pk_fp8_f32 v159, v50, v54
	v_cvt_pk_fp8_f32 v160, v3, v7
	v_cvt_pk_fp8_f32 v161, v19, v23
	v_cvt_pk_fp8_f32 v162, v35, v39
	v_cvt_pk_fp8_f32 v163, v51, v55
	v_cvt_pk_fp8_f32 v148, v8, v12 op_sel:[0,0,1]
	v_cvt_pk_fp8_f32 v149, v24, v28 op_sel:[0,0,1]
	v_cvt_pk_fp8_f32 v150, v40, v44 op_sel:[0,0,1]
	v_cvt_pk_fp8_f32 v151, v56, v60 op_sel:[0,0,1]
	v_cvt_pk_fp8_f32 v152, v9, v13 op_sel:[0,0,1]
	v_cvt_pk_fp8_f32 v153, v25, v29 op_sel:[0,0,1]
	v_cvt_pk_fp8_f32 v154, v41, v45 op_sel:[0,0,1]
	v_cvt_pk_fp8_f32 v155, v57, v61 op_sel:[0,0,1]
	v_cvt_pk_fp8_f32 v156, v10, v14 op_sel:[0,0,1]
	v_cvt_pk_fp8_f32 v157, v26, v30 op_sel:[0,0,1]
	v_cvt_pk_fp8_f32 v158, v42, v46 op_sel:[0,0,1]
	v_cvt_pk_fp8_f32 v159, v58, v62 op_sel:[0,0,1]
	v_cvt_pk_fp8_f32 v160, v11, v15 op_sel:[0,0,1]
	v_cvt_pk_fp8_f32 v161, v27, v31 op_sel:[0,0,1]
	v_cvt_pk_fp8_f32 v162, v43, v47 op_sel:[0,0,1]
	v_cvt_pk_fp8_f32 v163, v59, v63 op_sel:[0,0,1]
	s_movk_i32 s1, 0x200
	s_cmp_eq_u32 s14, 0
	s_cselect_b32 s0, 13, 11
	s_cselect_b32 s1, 0x800, s1
	v_lshlrev_b32_e32 v167, 4, v164
	v_lshl_add_u32 v167, v165, s0, v167
	global_store_dwordx4 v167, v[148:151], s[12:13] nt
	v_add_u32_e32 v167, s1, v167
	global_store_dwordx4 v167, v[152:155], s[12:13] nt
	v_add_u32_e32 v167, s1, v167
	global_store_dwordx4 v167, v[156:159], s[12:13] nt
	v_add_u32_e32 v167, s1, v167
	global_store_dwordx4 v167, v[160:163], s[12:13] nt
	s_nop 1
	s_add_u32 s68, s68, 1
	s_cmp_lt_u32 s68, 4
	s_cbranch_scc1 .Lcv_sl_cv1
	s_branch .LBB0_779

;     ...
;     int tid = tid_x(); asm volatile("" : "+v"(tid));
;     const int wid = tid >> 6, lane = tid & 63, r32 = lane & 31, hi = lane >> 5;
;     const int qb = uid & 15, h = (uid >> 4) % NH, b = (uid >> 4) / NH;
;     const int tok0 = b * SEQ;
;     const int qrow = tok0 + qb * 256 + wid * 32 + r32;
;     LAS char* V_lds = lds + LDS_VBUF; LAS char* K_lds = lds + LDS_KBUF;
;     LAS float* ws = (LAS float*)(lds + LDS_WS) + wid * 64; LAS float* li_l = ws; LAS float* al_l = ws + 32;
;     LAS float* rpbL = (LAS float*)(lds + LDS_RPB);
;     const int sr = tid >> 4, sc = (tid & 15) * 8, vst0 = v_st(sr, sc), vst1 = v_st(32 + sr, sc);
;     const int sr64 = tid >> 3, sc64 = (tid & 7) * 8;
;     const int vb0 = (int)(unsigned)(uintptr_t)V_lds + v_rd_base(lane);
;     int NT = 64, kbase = tok0;
;     int rq = 0, qc = 0, kr_lo = 0;
;     if constexpr (MODE == MODE_NA) { const int rq0 = qb * 4; kr_lo = min(min(max(rq0 - 4, 0), 56), 52); NT = 12; kbase = tok0 + kr_lo * 64; rq = rq0 + (wid >> 1); qc = (wid & 1) * 32 + r32;
;         for (int i = tid; i < 15 * 31; i += 512) rpbL[i] = P.rpb[h * 465 + i];
;         __syncthreads(); }
;     const bf16* Kg; const bf16* Vg; const bf16* Kg2 = nullptr; int ldk, ldv;
;     if constexpr (MODE == MODE_MLA) { Kg = P.KVM + h * 256; Vg = P.KVM + h * 256 + 128; Kg2 = P.U + U_KR; ldk = KVW; ldv = KVW; }
;     else if constexpr (MODE == MODE_NA) { Kg = P.U + U_NA + 512 + h * 128; Vg = P.U + U_NA + 1024 + h * 128; ldk = UW; ldv = UW; }
;     else { Kg = P.U + U_DF + 512 + h * 128; Vg = P.U + U_DF + 1024 + h * 128; ldk = UW; ldv = UW; }
;     constexpr int pass = PASS;
;     constexpr bool HALF_OFFSET = false;
;     {
;         float m_reg = -1e30f, l_reg = 0; f32x16 o[4] = {}; bf16x8 qr[NQ];
;         if constexpr (MODE == MODE_MLA) {
;             const bf16* Qw = P.QM + (size_t)qrow * QMW + h * 192 + hi * 8;
; #pragma unroll
;             for (int d0 = 0; d0 < 12; ++d0) qr[d0] = *(const bf16x8*)(Qw + d0 * 16);
;             const f32x2* rt = P.ropeM + (size_t)(qrow & (SEQ - 1)) * 32;
; #pragma unroll
;             for (int g = 0; g < 2; ++g) {
;                 bf16x8 x1 = qr[8 + g], x2 = qr[10 + g];
; #pragma unroll
;                 for (int e = 0; e < 8; ++e) { const f32x2 cs = rt[g * 16 + hi * 8 + e];
;                     const float a = bf2f((unsigned short)x1[e]), c = bf2f((unsigned short)x2[e]);
.LBB0_785:
	s_lshl_b32 s0, s22, 1
	s_and_b32 s0, s0, 14
	s_ashr_i32 s1, s22, 7
	s_add_i32 s0, s0, s1
	s_getreg_b32 s1, hwreg(HW_REG_HW_ID, 0, 6)
	s_and_b32 s1, s1, 63
	s_lshl_b32 s1, s1, 2
	s_add_i32 s1, s1, 0
	s_add_i32 s1, s1, 0x23f00
	s_waitcnt vmcnt(15)
	v_mov_b32_e32 v0, s1
	ds_read_b32 v0, v0
	v_mbcnt_lo_u32_b32 v1, -1, 0
	v_mbcnt_hi_u32_b32 v1, -1, v1
	v_mov_b32_e32 v145, v193
	v_mov_b32_e32 v149, v193
	s_movk_i32 s3, 0x70
	s_waitcnt lgkmcnt(0)
	v_readfirstlane_b32 s1, v0
	s_mov_b32 s28, 0
	v_mov_b32_e32 v147, v193
	s_waitcnt vmcnt(13)
	v_lshl_add_u32 v11, s1, 6, v1
	s_lshr_b32 s1, s0, 29
	s_add_i32 s1, s0, s1
	s_and_b32 s2, s1, -8
	s_sub_i32 s23, s0, s2
	s_lshl_b32 s0, s1, 9
	s_and_b32 s4, s0, 0xfffff000
	s_lshl_b32 s0, s22, 5
	s_and_b32 s0, s0, 0xf00
	s_or_b32 s25, s4, s0
	v_ashrrev_i32_e32 v156, 6, v11
	v_and_b32_e32 v154, 31, v11
	v_lshl_add_u32 v0, v156, 5, s25
	v_or_b32_e32 v8, v0, v154
	v_and_b32_e32 v0, 0x3fffffc0, v11
	s_add_i32 s0, 0, 0x1e000
	v_lshl_add_u32 v157, v0, 2, s0
	s_lshl_b32 s0, s23, 8
	s_ashr_i32 s1, s0, 31
	s_lshl_b64 s[0:1], s[0:1], 1
	s_add_u32 s26, s18, s0
	v_mov_b64_e32 v[0:1], s[10:11]
	s_movk_i32 s0, 0xc00
	s_addc_u32 s27, s19, s1
	v_mad_i64_i32 v[0:1], s[0:1], v8, s0, v[0:1]
	s_mul_i32 s0, s23, 0xc0
	v_lshlrev_b32_e32 v8, 8, v8
	v_bfe_u32 v155, v11, 5, 1
	s_ashr_i32 s1, s0, 31
	v_and_b32_e32 v192, 0xfff00, v8
	v_lshl_add_u64 v[0:1], s[0:1], 1, v[0:1]
	v_lshlrev_b32_e32 v144, 4, v155
	v_lshl_add_u64 v[8:9], s[12:13], 0, v[192:193]
	v_lshlrev_b32_e32 v192, 6, v155
	v_lshl_add_u64 v[4:5], v[0:1], 0, v[144:145]
	v_lshl_add_u64 v[8:9], v[8:9], 0, v[192:193]
	global_load_dwordx4 v[96:99], v[4:5], off
	global_load_dwordx4 v[100:103], v[4:5], off offset:32
	global_load_dwordx4 v[104:107], v[4:5], off offset:64
	global_load_dwordx4 v[108:111], v[4:5], off offset:96
	global_load_dwordx4 v[112:115], v[4:5], off offset:128
	global_load_dwordx4 v[116:119], v[4:5], off offset:160
	global_load_dwordx4 v[120:123], v[4:5], off offset:192
	global_load_dwordx4 v[124:127], v[4:5], off offset:224
	global_load_dwordx4 v[26:29], v[4:5], off offset:256
	global_load_dwordx4 v[0:3], v[4:5], off offset:288
	global_load_dwordx4 v[30:33], v[4:5], off offset:320
	s_nop 0
	global_load_dwordx4 v[4:7], v[4:5], off offset:352
	s_waitcnt vmcnt(24)
	v_lshlrev_b32_e32 v13, 4, v11
	global_load_dwordx2 v[14:15], v[8:9], off
	v_readfirstlane_b32 s0, v156
	s_ashr_i32 s5, s4, 31
	s_lshl_b32 s2, s0, 10
	s_lshl_b64 s[0:1], s[4:5], 12
	s_add_u32 s0, s26, s0
	s_addc_u32 s1, s27, s1
	s_add_i32 s29, s2, 0
	s_mov_b32 m0, s29
	s_add_i32 s2, s29, 0xc000
	v_and_b32_e32 v10, 63, v11
	v_and_b32_e32 v12, 0xc0, v13
	v_mov_b32_e32 v151, v193
	v_lshlrev_b32_e32 v145, 8, v154
	v_lshlrev_b32_e32 v167, 7, v154
	v_lshl_add_u32 v163, v154, 2, v157
	v_mov_b32_e32 v174, 0
	v_mov_b32_e32 v173, 0xf149f2ca
	s_waitcnt vmcnt(4)
	v_lshlrev_b32_e32 v17, 16, v26
	s_waitcnt vmcnt(2)
	v_lshlrev_b32_e32 v16, 16, v30
	s_waitcnt vmcnt(0)
	v_pk_mul_f32 v[18:19], v[14:15], v[16:17] op_sel:[0,1] op_sel_hi:[1,0]
	v_pk_mul_f32 v[14:15], v[14:15], v[16:17]
	v_sub_f32_e32 v18, v18, v19
	v_add_f32_e32 v14, v15, v14
	v_cvt_pk_bf16_f32 v15, v18, v193
	v_cvt_pk_bf16_f32 v14, v14, v193
	global_load_dwordx2 v[16:17], v[8:9], off offset:8
	v_and_b32_e32 v19, 0xffff0000, v26
	v_and_b32_e32 v18, 0xffff0000, v30
	s_waitcnt vmcnt(0)
	v_pk_mul_f32 v[20:21], v[16:17], v[18:19] op_sel:[0,1] op_sel_hi:[1,0]
	v_pk_mul_f32 v[16:17], v[16:17], v[18:19]
	v_sub_f32_e32 v20, v20, v21
	v_add_f32_e32 v16, v16, v17
	v_cvt_pk_bf16_f32 v17, v20, v193
	v_cvt_pk_bf16_f32 v16, v16, v193
	global_load_dwordx2 v[18:19], v[8:9], off offset:16
	v_lshlrev_b32_e32 v21, 16, v27
	v_lshlrev_b32_e32 v20, 16, v31
	s_waitcnt vmcnt(0)
	v_pk_mul_f32 v[22:23], v[18:19], v[20:21] op_sel:[0,1] op_sel_hi:[1,0]
	v_pk_mul_f32 v[18:19], v[18:19], v[20:21]
	v_sub_f32_e32 v22, v22, v23
	v_add_f32_e32 v18, v18, v19
	v_cvt_pk_bf16_f32 v19, v22, v193
	v_cvt_pk_bf16_f32 v18, v18, v193
	global_load_dwordx2 v[20:21], v[8:9], off offset:24
	v_and_b32_e32 v23, 0xffff0000, v27
	v_and_b32_e32 v22, 0xffff0000, v31
	s_waitcnt vmcnt(0)
	v_pk_mul_f32 v[24:25], v[20:21], v[22:23] op_sel:[0,1] op_sel_hi:[1,0]
	v_pk_mul_f32 v[20:21], v[20:21], v[22:23]
	v_sub_f32_e32 v24, v24, v25
	v_add_f32_e32 v20, v20, v21
	v_cvt_pk_bf16_f32 v21, v24, v193
	v_cvt_pk_bf16_f32 v20, v20, v193
	global_load_dwordx2 v[22:23], v[8:9], off offset:32
	v_lshlrev_b32_e32 v25, 16, v28
	v_lshlrev_b32_e32 v24, 16, v32
	s_waitcnt vmcnt(0)
	v_pk_mul_f32 v[26:27], v[22:23], v[24:25] op_sel:[0,1] op_sel_hi:[1,0]
	v_pk_mul_f32 v[22:23], v[22:23], v[24:25]
	v_sub_f32_e32 v26, v26, v27
	v_add_f32_e32 v22, v22, v23
	v_cvt_pk_bf16_f32 v23, v26, v193
	v_cvt_pk_bf16_f32 v22, v22, v193
	global_load_dwordx2 v[24:25], v[8:9], off offset:40
	v_and_b32_e32 v27, 0xffff0000, v28
	v_and_b32_e32 v26, 0xffff0000, v32
	s_waitcnt vmcnt(0)
	v_pk_mul_f32 v[30:31], v[24:25], v[26:27] op_sel:[0,1] op_sel_hi:[1,0]
	v_pk_mul_f32 v[24:25], v[24:25], v[26:27]
	v_sub_f32_e32 v28, v30, v31
	v_add_f32_e32 v24, v24, v25
	v_cvt_pk_bf16_f32 v25, v28, v193
	v_cvt_pk_bf16_f32 v24, v24, v193
	global_load_dwordx2 v[26:27], v[8:9], off offset:48
	v_lshlrev_b32_e32 v31, 16, v29
	v_lshlrev_b32_e32 v30, 16, v33
	v_and_b32_e32 v29, 0xffff0000, v29
	s_waitcnt vmcnt(0)
	v_pk_mul_f32 v[34:35], v[26:27], v[30:31] op_sel:[0,1] op_sel_hi:[1,0]
	v_pk_mul_f32 v[26:27], v[26:27], v[30:31]
	v_sub_f32_e32 v28, v34, v35
	v_add_f32_e32 v26, v26, v27
	v_cvt_pk_bf16_f32 v27, v28, v193
	v_cvt_pk_bf16_f32 v26, v26, v193
	global_load_dwordx2 v[30:31], v[8:9], off offset:56
	v_and_b32_e32 v28, 0xffff0000, v33
	v_lshlrev_b32_e32 v35, 16, v0
	v_lshlrev_b32_e32 v34, 16, v4
	s_waitcnt vmcnt(0)
; #define VM_WAIT() asm volatile("s_waitcnt vmcnt(0)" ::: "memory")
; __device__ __forceinline__ unsigned cvt_pk_bf16(float lo, float hi) { unsigned r; asm volatile("v_cvt_pk_bf16_f32 %0, %1, %2" : "=v"(r) : "v"(lo), "v"(hi)); return r; }
;     ...
;             const f32x2* rt = P.ropeM + (size_t)(qrow & (SEQ - 1)) * 32;
; #pragma unroll
;             for (int g = 0; g < 2; ++g) {
;                 bf16x8 x1 = qr[8 + g], x2 = qr[10 + g];
; #pragma unroll
;                 for (int e = 0; e < 8; ++e) { const f32x2 cs = rt[g * 16 + hi * 8 + e];
;                     const float a = bf2f((unsigned short)x1[e]), c = bf2f((unsigned short)x2[e]);
;                     const float ra = a * cs.x - c * cs.y, rc = c * cs.x + a * cs.y;
;                     x1[e] = (short)(cvt_pk_bf16(ra, 0.f) & 0xffffu); x2[e] = (short)(cvt_pk_bf16(rc, 0.f) & 0xffffu); }
;                 qr[8 + g] = x1; qr[10 + g] = x2;
;             }
;     ...
;         } else if constexpr (ATT_GLDS) {
;         unsigned gsv[2], gsk[2], gsk2 = 0u;
; #pragma unroll
;         for (int i = 0; i < 2; ++i) { const int a = (i * 512 + tid) * 16;
;             { const int sub = a >> 9, within = a & 511; const int kk = (sub >> 2) * 8 + (within >> 6); const int k = (kk & ~0xC) | ((kk & 4) << 1) | ((kk & 8) >> 1);
;               const int c = (sub & 3) * 32 + ((within & 63) >> 1); gsv[i] = (unsigned)(k * ldv + c) * 2u; }
;             if constexpr (MODE == MODE_DIFF) { if (i == 0) { const int row = a >> 7, ch = ((a >> 4) & 7) ^ ((row >> 1) & 7); gsk[0] = (unsigned)(row * ldk + ch * 8) * 2u; } gsk[1] = 0u; }
;             else { const int row = a >> 8, ch = ((a >> 4) & 15) ^ (row & 15); gsk[i] = (unsigned)(row * ldk + ch * 8) * 2u; } }
;         if constexpr (MODE == MODE_MLA) { const int a = tid * 16, row = a >> 7, ch = ((a >> 4) & 7) ^ ((row >> 1) & 7); gsk2 = (unsigned)(row * UW + ch * 8) * 2u; }
;         const unsigned ldsw = (unsigned)__builtin_amdgcn_readfirstlane(wid) * 1024u;
;     ...
;         GLDS(0, 0); VM_WAIT(); __syncthreads();
	v_pk_mul_f32 v[32:33], v[30:31], v[28:29] op_sel:[0,1] op_sel_hi:[1,0]
	v_pk_mul_f32 v[28:29], v[30:31], v[28:29]
	v_sub_f32_e32 v32, v32, v33
	v_add_f32_e32 v28, v28, v29
	v_cvt_pk_bf16_f32 v30, v32, v193
	v_cvt_pk_bf16_f32 v28, v28, v193
	global_load_dwordx2 v[32:33], v[8:9], off offset:128
	s_waitcnt vmcnt(0)
	v_pk_mul_f32 v[36:37], v[32:33], v[34:35] op_sel:[0,1] op_sel_hi:[1,0]
	v_pk_mul_f32 v[32:33], v[32:33], v[34:35]
	v_sub_f32_e32 v29, v36, v37
	v_add_f32_e32 v32, v32, v33
	v_cvt_pk_bf16_f32 v31, v29, v193
	v_cvt_pk_bf16_f32 v29, v32, v193
	global_load_dwordx2 v[32:33], v[8:9], off offset:136
	v_and_b32_e32 v35, 0xffff0000, v0
	v_and_b32_e32 v34, 0xffff0000, v4
	s_waitcnt vmcnt(0)
	v_pk_mul_f32 v[36:37], v[32:33], v[34:35] op_sel:[0,1] op_sel_hi:[1,0]
	v_pk_mul_f32 v[32:33], v[32:33], v[34:35]
	v_sub_f32_e32 v0, v36, v37
	v_add_f32_e32 v4, v32, v33
	v_cvt_pk_bf16_f32 v32, v0, v193
	v_cvt_pk_bf16_f32 v4, v4, v193
	global_load_dwordx2 v[34:35], v[8:9], off offset:144
	v_lshlrev_b32_e32 v37, 16, v1
	v_lshlrev_b32_e32 v36, 16, v5
	v_and_b32_e32 v1, 0xffff0000, v1
	s_waitcnt vmcnt(0)
	v_pk_mul_f32 v[38:39], v[34:35], v[36:37] op_sel:[0,1] op_sel_hi:[1,0]
	v_pk_mul_f32 v[34:35], v[34:35], v[36:37]
	v_sub_f32_e32 v0, v38, v39
	v_add_f32_e32 v33, v34, v35
	v_cvt_pk_bf16_f32 v34, v0, v193
	v_cvt_pk_bf16_f32 v33, v33, v193
	global_load_dwordx2 v[36:37], v[8:9], off offset:152
	v_and_b32_e32 v0, 0xffff0000, v5
	s_waitcnt vmcnt(0)
	v_pk_mul_f32 v[38:39], v[36:37], v[0:1] op_sel:[0,1] op_sel_hi:[1,0]
	v_pk_mul_f32 v[0:1], v[36:37], v[0:1]
	v_sub_f32_e32 v5, v38, v39
	v_add_f32_e32 v0, v0, v1
	v_cvt_pk_bf16_f32 v35, v5, v193
	v_cvt_pk_bf16_f32 v5, v0, v193
	global_load_dwordx2 v[0:1], v[8:9], off offset:160
	v_lshlrev_b32_e32 v37, 16, v2
	v_lshlrev_b32_e32 v36, 16, v6
	s_waitcnt vmcnt(0)
	v_pk_mul_f32 v[38:39], v[0:1], v[36:37] op_sel:[0,1] op_sel_hi:[1,0]
	v_pk_mul_f32 v[0:1], v[0:1], v[36:37]
	v_sub_f32_e32 v38, v38, v39
	v_add_f32_e32 v0, v0, v1
	v_cvt_pk_bf16_f32 v37, v38, v193
	v_cvt_pk_bf16_f32 v36, v0, v193
	global_load_dwordx2 v[0:1], v[8:9], off offset:168
	v_and_b32_e32 v39, 0xffff0000, v2
	v_and_b32_e32 v38, 0xffff0000, v6
	s_waitcnt vmcnt(0)
	v_pk_mul_f32 v[40:41], v[0:1], v[38:39] op_sel:[0,1] op_sel_hi:[1,0]
	v_pk_mul_f32 v[0:1], v[0:1], v[38:39]
	v_sub_f32_e32 v2, v40, v41
	v_add_f32_e32 v0, v0, v1
	v_cvt_pk_bf16_f32 v6, v2, v193
	v_cvt_pk_bf16_f32 v2, v0, v193
	global_load_dwordx2 v[0:1], v[8:9], off offset:176
	v_lshlrev_b32_e32 v39, 16, v3
	v_lshlrev_b32_e32 v38, 16, v7
	s_waitcnt vmcnt(0)
	v_pk_mul_f32 v[40:41], v[0:1], v[38:39] op_sel:[0,1] op_sel_hi:[1,0]
	v_pk_mul_f32 v[0:1], v[0:1], v[38:39]
	v_sub_f32_e32 v40, v40, v41
	v_add_f32_e32 v0, v0, v1
	v_cvt_pk_bf16_f32 v39, v40, v193
	v_cvt_pk_bf16_f32 v38, v0, v193
	global_load_dwordx2 v[0:1], v[8:9], off offset:184
	v_and_b32_e32 v9, 0xffff0000, v3
	v_and_b32_e32 v8, 0xffff0000, v7
	s_waitcnt vmcnt(0)
	v_pk_mul_f32 v[40:41], v[0:1], v[8:9] op_sel:[0,1] op_sel_hi:[1,0]
	v_pk_mul_f32 v[0:1], v[0:1], v[8:9]
	v_sub_f32_e32 v3, v40, v41
	v_add_f32_e32 v0, v0, v1
	v_bfe_i32 v9, v11, 4, 24
	v_cvt_pk_bf16_f32 v8, v3, v193
	v_cvt_pk_bf16_f32 v7, v0, v193
	v_bfe_u32 v0, v11, 2, 2
	v_lshrrev_b32_e32 v1, 1, v11
	v_lshlrev_b32_e32 v3, 1, v11
	v_lshrrev_b32_e32 v41, 1, v9
	v_and_or_b32 v0, v1, 8, v0
	v_and_b32_e32 v1, 0xc0, v3
	v_and_b32_e32 v40, 0xffff0, v9
	v_and_b32_e32 v41, 4, v41
	v_and_or_b32 v1, v13, 48, v1
	v_or3_b32 v40, v40, v41, v0
	v_lshl_or_b32 v192, v40, 12, v1
	v_xor_b32_e32 v40, v9, v11
	v_lshlrev_b32_e32 v9, 12, v9
	v_lshlrev_b32_e32 v40, 4, v40
	v_and_or_b32 v146, v40, s87, v9
	v_add_u32_e32 v9, 0x2000, v13
	v_ashrrev_i32_e32 v9, 8, v9
	v_lshrrev_b32_e32 v41, 1, v9
	v_and_b32_e32 v40, 0xffff0, v9
	v_and_b32_e32 v41, 4, v41
	v_or3_b32 v0, v40, v41, v0
	v_lshl_add_u64 v[40:41], s[0:1], 0, v[192:193]
	v_lshl_or_b32 v148, v0, 12, v1
	v_lshl_add_u64 v[40:41], v[40:41], 0, s[36:37]
	global_load_lds_dwordx4 v[40:41], off
	v_lshl_add_u64 v[40:41], s[0:1], 0, v[148:149]
	v_xor_b32_e32 v0, v9, v11
	v_lshl_add_u64 v[40:41], v[40:41], 0, s[36:37]
	s_add_i32 m0, s29, 0x2000
	v_lshlrev_b32_e32 v1, 12, v9
	v_lshlrev_b32_e32 v0, 4, v0
	global_load_lds_dwordx4 v[40:41], off
	s_mov_b32 m0, s2
	v_and_or_b32 v150, v0, s87, v1
	global_load_lds_dwordx4 v146, s[0:1]
	s_add_i32 m0, s29, 0xe000
	v_lshlrev_b32_e32 v0, 10, v11
	global_load_lds_dwordx4 v150, s[0:1]
	s_lshl_b64 s[0:1], s[4:5], 13
	v_and_b32_e32 v0, 0xffffe000, v0
	v_xor_b32_e32 v1, v13, v11
	s_add_u32 s0, s14, s0
	v_and_or_b32 v0, v1, s3, v0
	s_addc_u32 s1, s15, s1
	s_add_i32 m0, s29, 0x10000
	v_mov_b32_e32 v1, v193
	global_load_lds_dwordx4 v0, s[0:1]
	v_lshl_add_u64 v[152:153], s[14:15], 0, v[0:1]
	v_bitop3_b32 v0, v155, v11, 15 bitop3:0x78
	v_lshlrev_b32_e32 v9, 3, v11
	v_lshlrev_b32_e32 v158, 4, v0
	v_and_b32_e32 v0, 0xf0, v13
	v_bitop3_b32 v159, v144, v0, 32 bitop3:0x36
	v_bitop3_b32 v160, v144, v0, 64 bitop3:0x36
	v_bitop3_b32 v161, v144, v0, s60 bitop3:0x36
	v_bitop3_b32 v162, v144, v0, s59 bitop3:0x36
	v_bitop3_b32 v164, v144, v0, s61 bitop3:0x36
	v_bitop3_b32 v165, v144, v0, s58 bitop3:0x36
	v_bitop3_b32 v166, v144, v0, s62 bitop3:0x36
	v_and_b32_e32 v0, 0x70, v9
	v_bitop3_b32 v169, v144, v0, 32 bitop3:0x36
	v_bitop3_b32 v170, v144, v0, 64 bitop3:0x36
	v_bitop3_b32 v171, v144, v0, s60 bitop3:0x36
	v_and_b32_e32 v0, 0x118, v9
	s_mov_b32 s0, 0x5040100
	s_waitcnt vmcnt(0)
; #define VM_WAIT() asm volatile("s_waitcnt vmcnt(0)" ::: "memory")
; #define SBAR() __builtin_amdgcn_sched_barrier(0)
; #define NAMASK(pa_, pb_, t) do { if constexpr (MODE == MODE_NA) na_bias_mask(pa_, pb_, rpbL, kr_lo + (t), rq, qc, hi); } while (0)
;     ...
;         } else if constexpr (ATT_GLDS) {
;         unsigned gsv[2], gsk[2], gsk2 = 0u;
; #pragma unroll
;         for (int i = 0; i < 2; ++i) { const int a = (i * 512 + tid) * 16;
;             { const int sub = a >> 9, within = a & 511; const int kk = (sub >> 2) * 8 + (within >> 6); const int k = (kk & ~0xC) | ((kk & 4) << 1) | ((kk & 8) >> 1);
;               const int c = (sub & 3) * 32 + ((within & 63) >> 1); gsv[i] = (unsigned)(k * ldv + c) * 2u; }
;             if constexpr (MODE == MODE_DIFF) { if (i == 0) { const int row = a >> 7, ch = ((a >> 4) & 7) ^ ((row >> 1) & 7); gsk[0] = (unsigned)(row * ldk + ch * 8) * 2u; } gsk[1] = 0u; }
;             else { const int row = a >> 8, ch = ((a >> 4) & 15) ^ (row & 15); gsk[i] = (unsigned)(row * ldk + ch * 8) * 2u; } }
;         if constexpr (MODE == MODE_MLA) { const int a = tid * 16, row = a >> 7, ch = ((a >> 4) & 7) ^ ((row >> 1) & 7); gsk2 = (unsigned)(row * UW + ch * 8) * 2u; }
;         const unsigned ldsw = (unsigned)__builtin_amdgcn_readfirstlane(wid) * 1024u;
;     ...
;         GLDS(0, 0); VM_WAIT(); __syncthreads();
; #pragma unroll 1
;         for (int t = 0; t < NT; ++t) {
;             const int bf = t & 1;
;             if (t + 1 < NT) GLDS(t + 1, bf ^ 1);
;             SBAR();
;             bool act = true;
;             if constexpr (MODE == MODE_NA) { const int kr = kr_lo + t, r0w = min(max(rq - 4, 0), 56); act = (kr >= r0w) && (kr < r0w + 8); }
;             if (act) {
;             qkt<MODE>(p0, p1, K_lds + bf * SHM_K, qr, r32, hi); NAMASK(p0, p1, t);
	v_perm_b32 v128, v17, v15, s0
	v_perm_b32 v136, v16, v14, s0
	v_and_or_b32 v0, v3, 32, v0
	v_mov_b32_e32 v14, v193
	v_mov_b32_e32 v15, v193
	v_bitop3_b32 v168, v144, v9, s3 bitop3:0x78
	v_cmp_gt_u32_e64 s[2:3], 32, v10
	v_perm_b32 v129, v21, v19, s0
	v_perm_b32 v130, v25, v23, s0
	v_perm_b32 v131, v30, v27, s0
	v_perm_b32 v132, v32, v31, s0
	v_perm_b32 v133, v35, v34, s0
	v_perm_b32 v134, v6, v37, s0
	v_perm_b32 v135, v8, v39, s0
	v_perm_b32 v137, v20, v18, s0
	v_perm_b32 v138, v24, v22, s0
	v_perm_b32 v139, v28, v26, s0
	v_perm_b32 v140, v4, v29, s0
	v_perm_b32 v141, v5, v33, s0
	v_perm_b32 v142, v2, v36, s0
	v_perm_b32 v143, v7, v38, s0
	v_add3_u32 v172, v12, 0, v0
	v_mov_b32_e32 v0, v193
	v_mov_b32_e32 v2, v193
	v_mov_b32_e32 v3, v193
	v_mov_b32_e32 v4, v193
	v_mov_b32_e32 v5, v193
	v_mov_b32_e32 v6, v193
	v_mov_b32_e32 v7, v193
	v_mov_b32_e32 v8, v193
	v_mov_b32_e32 v9, v193
	v_mov_b32_e32 v10, v193
	v_mov_b32_e32 v11, v193
	v_mov_b32_e32 v12, v193
	v_mov_b32_e32 v13, v193
	v_mov_b64_e32 v[30:31], v[14:15]
	v_mov_b64_e32 v[46:47], v[14:15]
	v_mov_b64_e32 v[62:63], v[14:15]
	s_or_b32 s16, s4, 64
	v_mov_b64_e32 v[28:29], v[12:13]
	v_mov_b64_e32 v[26:27], v[10:11]
	v_mov_b64_e32 v[24:25], v[8:9]
	v_mov_b64_e32 v[22:23], v[6:7]
	v_mov_b64_e32 v[20:21], v[4:5]
	v_mov_b64_e32 v[18:19], v[2:3]
	v_mov_b64_e32 v[16:17], v[0:1]
	v_mov_b64_e32 v[44:45], v[12:13]
	v_mov_b64_e32 v[42:43], v[10:11]
	v_mov_b64_e32 v[40:41], v[8:9]
	v_mov_b64_e32 v[38:39], v[6:7]
	v_mov_b64_e32 v[36:37], v[4:5]
	v_mov_b64_e32 v[34:35], v[2:3]
	v_mov_b64_e32 v[32:33], v[0:1]
	v_mov_b64_e32 v[60:61], v[12:13]
	v_mov_b64_e32 v[58:59], v[10:11]
	v_mov_b64_e32 v[56:57], v[8:9]
	v_mov_b64_e32 v[54:55], v[6:7]
	v_mov_b64_e32 v[52:53], v[4:5]
	v_mov_b64_e32 v[50:51], v[2:3]
	v_mov_b64_e32 v[48:49], v[0:1]
	s_waitcnt vmcnt(0) lgkmcnt(0)
	s_barrier
	s_and_b32 s30, s28, 1
	s_cmp_eq_u32 s28, 63
	s_cbranch_scc1 .LBB0_788
	s_branch .LBB0_787
.LBB0_786:
	v_mov_b32_e32 v174, v64
	s_and_b32 s30, s28, 1
	s_cmp_eq_u32 s28, 63
	s_cbranch_scc1 .LBB0_788
.LBB0_787:
	s_ashr_i32 s17, s16, 31
	s_lshl_b64 s[0:1], s[16:17], 12
	s_add_u32 s0, s26, s0
	s_addc_u32 s1, s27, s1
	s_xor_b32 s4, s30, 1
	s_lshl_b32 s5, s4, 14
	s_add_i32 s5, s29, s5
	v_lshl_add_u64 v[64:65], s[0:1], 0, v[192:193]
	s_mulk_i32 s4, 0x6000
	v_lshl_add_u64 v[64:65], v[64:65], 0, s[36:37]
	s_mov_b32 m0, s5
	s_add_i32 s4, s29, s4
	global_load_lds_dwordx4 v[64:65], off
	v_lshl_add_u64 v[64:65], s[0:1], 0, v[148:149]
	s_add_i32 s31, s4, 0xc000
	v_lshl_add_u64 v[64:65], v[64:65], 0, s[36:37]
	s_add_i32 m0, s5, 0x2000
	s_nop 0
	global_load_lds_dwordx4 v[64:65], off
	v_lshl_add_u64 v[64:65], s[0:1], 0, v[146:147]
	s_mov_b32 m0, s31
	s_nop 0
	global_load_lds_dwordx4 v[64:65], off
	v_lshl_add_u64 v[64:65], s[0:1], 0, v[150:151]
	s_add_i32 m0, s4, 0xe000
	s_lshl_b64 s[0:1], s[16:17], 13
	global_load_lds_dwordx4 v[64:65], off
	v_lshl_add_u64 v[64:65], v[152:153], 0, s[0:1]
	s_add_i32 m0, s4, 0x10000
	s_nop 0
	global_load_lds_dwordx4 v[64:65], off

; template <int MODE>
; __device__ __forceinline__ void partialSM(f32x16& p0, f32x16& p1, float& m_reg, float& mn, float& alpha) {
;     ...
;     else { mn = fmaxf(m_reg, pmax); alpha = __builtin_amdgcn_exp2f((m_reg - mn) * C); m_reg = mn; }
;     const float mnC = -mn * C;
; #pragma unroll
;     for (int r = 0; r < 16; ++r) p0[r] = fmaf(p0[r], C, mnC);
; #pragma unroll
;     for (int r = 0; r < 16; ++r) p1[r] = fmaf(p1[r], C, mnC);
; #pragma unroll
;     for (int r = 0; r < 16; ++r) p0[r] = __builtin_amdgcn_exp2f(p0[r]);
; }
; __device__ __forceinline__ void finishSM(f32x16& p0, f32x16& p1, float alpha, float& l_reg, bf16x8& pa0, bf16x8& pa1, bf16x8& pa2, bf16x8& pa3) {
; #pragma unroll
;     for (int r = 0; r < 16; ++r) p1[r] = __builtin_amdgcn_exp2f(p1[r]);
;     float ps = 0;
; #pragma unroll
;     for (int r = 0; r < 16; ++r) ps += p0[r];
; #pragma unroll
;     for (int r = 0; r < 16; ++r) ps += p1[r];
;     { auto rr = __builtin_amdgcn_permlane32_swap(__float_as_uint(ps), __float_as_uint(ps), false, false);
;       ps = __uint_as_float(rr[0]) + __uint_as_float(rr[1]); }
;     l_reg = l_reg * alpha + ps;
;     ...
;     PK4(p0, 0, pa0); PK4(p0, 8, pa1); PK4(p1, 0, pa2); PK4(p1, 8, pa3);
;     ...
; }
; template <int OFF> __device__ __forceinline__ s16x4 tr_read(int vb) {
;     s16x4 r; asm volatile("ds_read_b64_tr_b16 %0, %1 offset:%2" : "=&v"(r) : "v"(vb), "i"(OFF) : "memory"); return r;
; }
; template <int D0> __device__ __forceinline__ void pv_one(f32x16& od, int vb, bf16x8 pa0, bf16x8 pa1, bf16x8 pa2, bf16x8 pa3) {
;     const s16x4 l0 = tr_read<v_rd_off(D0, 0, 0)>(vb), h0 = tr_read<v_rd_off(D0, 0, 1)>(vb), l1 = tr_read<v_rd_off(D0, 1, 0)>(vb), h1 = tr_read<v_rd_off(D0, 1, 1)>(vb);
;     const s16x4 l2 = tr_read<v_rd_off(D0, 2, 0)>(vb), h2 = tr_read<v_rd_off(D0, 2, 1)>(vb), l3 = tr_read<v_rd_off(D0, 3, 0)>(vb), h3 = tr_read<v_rd_off(D0, 3, 1)>(vb);
;     asm volatile("s_waitcnt lgkmcnt(0)" ::: "memory"); SBAR();
;     ...
;     od = __builtin_amdgcn_mfma_f32_32x32x16_bf16(pa0, PK(l0, h0), od, 0, 0, 0);
;     od = __builtin_amdgcn_mfma_f32_32x32x16_bf16(pa1, PK(l1, h1), od, 0, 0, 0);
;     od = __builtin_amdgcn_mfma_f32_32x32x16_bf16(pa2, PK(l2, h2), od, 0, 0, 0);
;     od = __builtin_amdgcn_mfma_f32_32x32x16_bf16(pa3, PK(l3, h3), od, 0, 0, 0);
;     ...
; }
; __device__ __forceinline__ void pv_d0(f32x16* o, int vb, bf16x8 pa0, bf16x8 pa1, bf16x8 pa2, bf16x8 pa3) {
.LBB0_792:
	v_cndmask_b32_e64 v173, v176, v173, s[4:5]
	v_mul_f32_e32 v176, 0xbdd53b94, v173
	v_fmamk_f32 v80, v80, 0x3dd53b94, v176
	v_fmamk_f32 v81, v81, 0x3dd53b94, v176
	v_fmamk_f32 v82, v82, 0x3dd53b94, v176
	v_fmamk_f32 v83, v83, 0x3dd53b94, v176
	v_fmamk_f32 v84, v84, 0x3dd53b94, v176
	v_fmamk_f32 v85, v85, 0x3dd53b94, v176
	v_fmamk_f32 v86, v86, 0x3dd53b94, v176
	v_fmamk_f32 v87, v87, 0x3dd53b94, v176
	v_fmamk_f32 v88, v88, 0x3dd53b94, v176
	v_fmamk_f32 v89, v89, 0x3dd53b94, v176
	v_fmamk_f32 v90, v90, 0x3dd53b94, v176
	v_fmamk_f32 v91, v91, 0x3dd53b94, v176
	v_fmamk_f32 v92, v92, 0x3dd53b94, v176
	v_fmamk_f32 v93, v93, 0x3dd53b94, v176
	v_fmamk_f32 v94, v94, 0x3dd53b94, v176
	v_fmamk_f32 v95, v95, 0x3dd53b94, v176
	v_fmamk_f32 v64, v64, 0x3dd53b94, v176
	v_fmamk_f32 v65, v65, 0x3dd53b94, v176
	v_fmamk_f32 v66, v66, 0x3dd53b94, v176
	v_fmamk_f32 v67, v67, 0x3dd53b94, v176
	v_fmamk_f32 v68, v68, 0x3dd53b94, v176
	v_fmamk_f32 v69, v69, 0x3dd53b94, v176
	v_fmamk_f32 v70, v70, 0x3dd53b94, v176
	v_fmamk_f32 v71, v71, 0x3dd53b94, v176
	v_fmamk_f32 v72, v72, 0x3dd53b94, v176
	v_fmamk_f32 v73, v73, 0x3dd53b94, v176
	v_fmamk_f32 v74, v74, 0x3dd53b94, v176
	v_fmamk_f32 v75, v75, 0x3dd53b94, v176
	v_fmamk_f32 v76, v76, 0x3dd53b94, v176
	v_fmamk_f32 v77, v77, 0x3dd53b94, v176
	v_fmamk_f32 v78, v78, 0x3dd53b94, v176
	v_fmac_f32_e32 v176, 0x3dd53b94, v79
	v_exp_f32_e32 v79, v80
	v_exp_f32_e32 v80, v81
	v_exp_f32_e32 v81, v82
	v_exp_f32_e32 v82, v83
	v_exp_f32_e32 v83, v84
	v_exp_f32_e32 v84, v85
	v_exp_f32_e32 v85, v86
	v_exp_f32_e32 v86, v87
	v_exp_f32_e32 v87, v88
	v_exp_f32_e32 v88, v89
	v_exp_f32_e32 v89, v90
	v_exp_f32_e32 v90, v91
	v_exp_f32_e32 v91, v92
	v_exp_f32_e32 v92, v93
	v_exp_f32_e32 v93, v94
	v_exp_f32_e32 v94, v95
	v_exp_f32_e32 v95, v64
	v_add_f32_e32 v64, 0, v79
	v_add_f32_e32 v64, v80, v64
	v_add_f32_e32 v64, v81, v64
	v_add_f32_e32 v64, v82, v64
	v_add_f32_e32 v64, v83, v64
	v_add_f32_e32 v64, v84, v64
	v_add_f32_e32 v64, v85, v64
	v_add_f32_e32 v64, v86, v64
	v_add_f32_e32 v64, v87, v64
	v_add_f32_e32 v64, v88, v64
	v_add_f32_e32 v64, v89, v64
	v_add_f32_e32 v64, v90, v64
	v_add_f32_e32 v64, v91, v64
	v_exp_f32_e32 v65, v65
	v_add_f32_e32 v64, v92, v64
	v_exp_f32_e32 v177, v66
	v_add_f32_e32 v64, v93, v64
	v_exp_f32_e32 v178, v67
	v_add_f32_e32 v64, v94, v64
	v_exp_f32_e32 v179, v68
	v_add_f32_e32 v64, v95, v64
	v_exp_f32_e32 v180, v69
	v_add_f32_e32 v64, v65, v64
	v_exp_f32_e32 v181, v70
	v_add_f32_e32 v64, v177, v64
	v_exp_f32_e32 v182, v71
	v_add_f32_e32 v64, v178, v64
	v_exp_f32_e32 v183, v72
	v_add_f32_e32 v64, v179, v64
	v_exp_f32_e32 v184, v73
	v_add_f32_e32 v64, v180, v64
	v_exp_f32_e32 v185, v74
	v_add_f32_e32 v64, v181, v64
	v_exp_f32_e32 v186, v75
	v_add_f32_e32 v64, v182, v64
	v_exp_f32_e32 v187, v76
	v_add_f32_e32 v64, v183, v64
	v_exp_f32_e32 v188, v77
	v_add_f32_e32 v64, v184, v64
	v_exp_f32_e32 v189, v78
	v_add_f32_e32 v64, v185, v64
	v_exp_f32_e32 v176, v176
	v_add_f32_e32 v64, v186, v64
	v_add_f32_e32 v64, v187, v64
	v_add_f32_e32 v64, v188, v64
	v_add_f32_e32 v64, v189, v64
	v_add_f32_e32 v64, v176, v64
	v_mov_b32_e32 v66, v64
	s_nop 1
	v_permlane32_swap_b32_e32 v64, v66
	v_add_f32_e32 v64, v64, v66
	s_add_i32 s28, s28, 1
	v_fmac_f32_e32 v64, v174, v175
	v_cvt_pk_bf16_f32 v66, v79, v80
	v_cvt_pk_bf16_f32 v67, v81, v82
	v_cvt_pk_bf16_f32 v68, v83, v84
	v_cvt_pk_bf16_f32 v69, v85, v86
	v_cvt_pk_bf16_f32 v70, v87, v88
	v_cvt_pk_bf16_f32 v71, v89, v90
	v_cvt_pk_bf16_f32 v72, v91, v92
	v_cvt_pk_bf16_f32 v73, v93, v94
	v_cvt_pk_bf16_f32 v74, v95, v65
	v_cvt_pk_bf16_f32 v75, v177, v178
	v_cvt_pk_bf16_f32 v76, v179, v180
	v_cvt_pk_bf16_f32 v77, v181, v182
	v_cvt_pk_bf16_f32 v78, v183, v184
	v_cvt_pk_bf16_f32 v79, v185, v186
	v_cvt_pk_bf16_f32 v80, v187, v188
	v_cvt_pk_bf16_f32 v81, v189, v176
	s_nop 0
	v_permlane32_swap_b32_e32 v66, v68
	v_permlane32_swap_b32_e32 v67, v69
	v_permlane32_swap_b32_e32 v70, v72
	v_permlane32_swap_b32_e32 v71, v73
	v_permlane32_swap_b32_e32 v74, v76
	v_permlane32_swap_b32_e32 v75, v77
	v_permlane32_swap_b32_e32 v78, v80
	v_permlane32_swap_b32_e32 v79, v81
	v_lshl_add_u32 v65, s30, 14, v172
	ds_read_b64_tr_b16 v[82:83], v65 offset:0
	ds_read_b64_tr_b16 v[84:85], v65 offset:0x800
	ds_read_b64_tr_b16 v[86:87], v65 offset:0x1000
	ds_read_b64_tr_b16 v[88:89], v65 offset:0x1800
	ds_read_b64_tr_b16 v[90:91], v65 offset:0x2000
	ds_read_b64_tr_b16 v[92:93], v65 offset:0x2800
	ds_read_b64_tr_b16 v[174:175], v65 offset:0x3000
	ds_read_b64_tr_b16 v[176:177], v65 offset:0x3800
	s_waitcnt lgkmcnt(0)
	s_nop 0
	v_mfma_f32_32x32x16_bf16 v[0:15], v[66:69], v[82:85], v[0:15]
	ds_read_b64_tr_b16 v[82:83], v65 offset:0x200
	ds_read_b64_tr_b16 v[84:85], v65 offset:0xa00
	v_mfma_f32_32x32x16_bf16 v[0:15], v[70:73], v[86:89], v[0:15]
	ds_read_b64_tr_b16 v[86:87], v65 offset:0x1200
	ds_read_b64_tr_b16 v[88:89], v65 offset:0x1a00
	v_mfma_f32_32x32x16_bf16 v[0:15], v[74:77], v[90:93], v[0:15]
	ds_read_b64_tr_b16 v[90:91], v65 offset:0x2200
	ds_read_b64_tr_b16 v[92:93], v65 offset:0x2a00
	v_mfma_f32_32x32x16_bf16 v[0:15], v[78:81], v[174:177], v[0:15]
	ds_read_b64_tr_b16 v[174:175], v65 offset:0x3200
	ds_read_b64_tr_b16 v[176:177], v65 offset:0x3a00
	s_waitcnt lgkmcnt(0)
	v_mfma_f32_32x32x16_bf16 v[16:31], v[66:69], v[82:85], v[16:31]
	ds_read_b64_tr_b16 v[82:83], v65 offset:0x400
	ds_read_b64_tr_b16 v[84:85], v65 offset:0xc00
	v_mfma_f32_32x32x16_bf16 v[16:31], v[70:73], v[86:89], v[16:31]
	ds_read_b64_tr_b16 v[86:87], v65 offset:0x1400
	ds_read_b64_tr_b16 v[88:89], v65 offset:0x1c00
	v_mfma_f32_32x32x16_bf16 v[16:31], v[74:77], v[90:93], v[16:31]
	ds_read_b64_tr_b16 v[90:91], v65 offset:0x2400
	ds_read_b64_tr_b16 v[92:93], v65 offset:0x2c00
	v_mfma_f32_32x32x16_bf16 v[16:31], v[78:81], v[174:177], v[16:31]
	ds_read_b64_tr_b16 v[174:175], v65 offset:0x3400
	ds_read_b64_tr_b16 v[176:177], v65 offset:0x3c00
	s_waitcnt lgkmcnt(0)
	v_mfma_f32_32x32x16_bf16 v[32:47], v[66:69], v[82:85], v[32:47]
	ds_read_b64_tr_b16 v[82:83], v65 offset:0x600
	ds_read_b64_tr_b16 v[84:85], v65 offset:0xe00
	v_mfma_f32_32x32x16_bf16 v[32:47], v[70:73], v[86:89], v[32:47]
	ds_read_b64_tr_b16 v[86:87], v65 offset:0x1600
	ds_read_b64_tr_b16 v[88:89], v65 offset:0x1e00
	v_mfma_f32_32x32x16_bf16 v[32:47], v[74:77], v[90:93], v[32:47]
	ds_read_b64_tr_b16 v[90:91], v65 offset:0x2600
	ds_read_b64_tr_b16 v[92:93], v65 offset:0x2e00
	v_mfma_f32_32x32x16_bf16 v[32:47], v[78:81], v[174:177], v[32:47]
	ds_read_b64_tr_b16 v[174:175], v65 offset:0x3600
	ds_read_b64_tr_b16 v[176:177], v65 offset:0x3e00
	s_waitcnt lgkmcnt(0)
	v_mfma_f32_32x32x16_bf16 v[48:63], v[66:69], v[82:85], v[48:63]
	s_waitcnt vmcnt(0)
	s_add_i32 s16, s16, 64
	s_cmp_eq_u32 s28, 64
	s_waitcnt vmcnt(0)
	s_barrier
	v_mfma_f32_32x32x16_bf16 v[48:63], v[70:73], v[86:89], v[48:63]
	v_mfma_f32_32x32x16_bf16 v[48:63], v[74:77], v[90:93], v[48:63]
	v_mfma_f32_32x32x16_bf16 v[48:63], v[78:81], v[174:177], v[48:63]
	s_cbranch_scc0 .LBB0_786
	s_and_saveexec_b64 s[0:1], s[2:3]
	s_cbranch_execz .LBB0_784
	ds_write_b32 v163, v64
	s_branch .LBB0_784

; __global__ void __launch_bounds__(512, 2) mk_fwd(Args args) {
;     extern __shared__ __attribute__((aligned(16))) unsigned char lds_raw[];
	.amdhsa_kernel _Z6mk_fwd4Args
		.amdhsa_group_segment_fixed_size 0
		.amdhsa_private_segment_fixed_size 0
		.amdhsa_kernarg_size 504
		.amdhsa_user_sgpr_count 2
		.amdhsa_user_sgpr_dispatch_ptr 0
		.amdhsa_user_sgpr_queue_ptr 0
		.amdhsa_user_sgpr_kernarg_segment_ptr 1
		.amdhsa_user_sgpr_dispatch_id 0
		.amdhsa_user_sgpr_kernarg_preload_length 0
		.amdhsa_user_sgpr_kernarg_preload_offset 0
		.amdhsa_user_sgpr_private_segment_size 0
		.amdhsa_uses_dynamic_stack 0
		.amdhsa_enable_private_segment 0
		.amdhsa_system_sgpr_workgroup_id_x 1
		.amdhsa_system_sgpr_workgroup_id_y 0
		.amdhsa_system_sgpr_workgroup_id_z 0
		.amdhsa_system_sgpr_workgroup_info 0
		.amdhsa_system_vgpr_workitem_id 0
		.amdhsa_next_free_vgpr 256
		.amdhsa_next_free_sgpr 102
		.amdhsa_accum_offset 256
		.amdhsa_reserve_vcc 1
		.amdhsa_float_round_mode_32 0
		.amdhsa_float_round_mode_16_64 0
		.amdhsa_float_denorm_mode_32 3
		.amdhsa_float_denorm_mode_16_64 3
		.amdhsa_dx10_clamp 1
		.amdhsa_ieee_mode 1
		.amdhsa_fp16_overflow 0
		.amdhsa_tg_split 0
		.amdhsa_exception_fp_ieee_invalid_op 0
		.amdhsa_exception_fp_denorm_src 0
		.amdhsa_exception_fp_ieee_div_zero 0
		.amdhsa_exception_fp_ieee_overflow 0
		.amdhsa_exception_fp_ieee_underflow 0
		.amdhsa_exception_fp_ieee_inexact 0
		.amdhsa_exception_int_div_zero 0
	.end_amdhsa_kernel

; __global__ void __launch_bounds__(512, 2) mk_fwd(Args args) {
;     extern __shared__ __attribute__((aligned(16))) unsigned char lds_raw[];
amdhsa.kernels:
  - .agpr_count:     0
    .args:
      - .offset:         0
        .size:           248
        .value_kind:     by_value
      - .offset:         248
        .size:           4
        .value_kind:     hidden_block_count_x
      - .offset:         252
        .size:           4
        .value_kind:     hidden_block_count_y
      - .offset:         256
        .size:           4
        .value_kind:     hidden_block_count_z
      - .offset:         260
        .size:           2
        .value_kind:     hidden_group_size_x
      - .offset:         262
        .size:           2
        .value_kind:     hidden_group_size_y
      - .offset:         264
        .size:           2
        .value_kind:     hidden_group_size_z
      - .offset:         266
        .size:           2
        .value_kind:     hidden_remainder_x
      - .offset:         268
        .size:           2
        .value_kind:     hidden_remainder_y
      - .offset:         270
        .size:           2
        .value_kind:     hidden_remainder_z
      - .offset:         288
        .size:           8
        .value_kind:     hidden_global_offset_x
      - .offset:         296
        .size:           8
        .value_kind:     hidden_global_offset_y
      - .offset:         304
        .size:           8
        .value_kind:     hidden_global_offset_z
      - .offset:         312
        .size:           2
        .value_kind:     hidden_grid_dims
      - .offset:         368
        .size:           4
        .value_kind:     hidden_dynamic_lds_size
    .group_segment_fixed_size: 0
    .kernarg_segment_align: 8
    .kernarg_segment_size: 504
    .language:       OpenCL C
    .language_version:
      - 2
      - 0
    .max_flat_workgroup_size: 512
    .name:           _Z6mk_fwd4Args
    .private_segment_fixed_size: 0
    .sgpr_count:     108
    .sgpr_spill_count: 103
    .symbol:         _Z6mk_fwd4Args.kd
    .uniform_work_group_size: 1
    .uses_dynamic_stack: false
    .vgpr_count:     256
    .vgpr_spill_count: 0
    .wavefront_size: 64
